# GEMM K-loops (P2,P8,P19): loop-invariant B-fragment LDS bases hoisted out of the loop (two loader-segment VALU per iteration removed); on top of v062
# speedup vs baseline: 1.0053x; 1.0032x over previous
.LBB0_201:
	s_ashr_i32 s21, s20, 31
	v_cmp_lt_i64_e32 vcc, s[22:23], v[158:159]
	s_lshl_b64 s[22:23], s[20:21], 19
	v_readlane_b32 s11, v254, 36
	s_add_u32 s22, s11, s22
	v_readlane_b32 s11, v254, 37
	s_addc_u32 s23, s11, s23
	s_and_b64 s[26:27], vcc, exec
	s_cselect_b32 s21, s23, s31
	s_cselect_b32 s52, s22, s30
	s_ashr_i32 s11, s10, 31
	s_lshl_b64 s[26:27], s[10:11], 19
	s_add_u32 s26, s9, s26
	s_addc_u32 s27, s33, s27
	s_and_b64 s[36:37], vcc, exec
	s_cselect_b32 s11, s27, s35
	s_cselect_b32 s53, s26, s34
	s_add_u32 s30, s30, 0x40080
	s_addc_u32 s31, s31, 0
	s_add_u32 s54, s34, 0x100
	v_mov_b32_e32 v18, 0
	s_addc_u32 s55, s35, 0
	s_mov_b32 s56, -2
	v_mov_b32_e32 v19, v18
	v_mov_b32_e32 v20, v18
	v_mov_b32_e32 v21, v18
	v_mov_b32_e32 v22, v18
	v_mov_b32_e32 v23, v18
	v_mov_b32_e32 v24, v18
	v_mov_b32_e32 v25, v18
	v_mov_b32_e32 v26, v18
	v_mov_b32_e32 v27, v18
	v_mov_b32_e32 v28, v18
	v_mov_b32_e32 v29, v18
	v_mov_b32_e32 v34, v18
	v_mov_b32_e32 v35, v18
	v_mov_b32_e32 v36, v18
	v_mov_b32_e32 v37, v18
	v_mov_b32_e32 v42, v18
	v_mov_b32_e32 v43, v18
	v_mov_b32_e32 v44, v18
	v_mov_b32_e32 v45, v18
	v_mov_b32_e32 v50, v18
	v_mov_b32_e32 v51, v18
	v_mov_b32_e32 v52, v18
	v_mov_b32_e32 v53, v18
	v_mov_b32_e32 v58, v18
	v_mov_b32_e32 v59, v18
	v_mov_b32_e32 v60, v18
	v_mov_b32_e32 v61, v18
	v_mov_b32_e32 v66, v18
	v_mov_b32_e32 v67, v18
	v_mov_b32_e32 v68, v18
	v_mov_b32_e32 v69, v18
	v_mov_b32_e32 v30, v18
	v_mov_b32_e32 v31, v18
	v_mov_b32_e32 v32, v18
	v_mov_b32_e32 v33, v18
	v_mov_b32_e32 v38, v18
	v_mov_b32_e32 v39, v18
	v_mov_b32_e32 v40, v18
	v_mov_b32_e32 v41, v18
	v_mov_b32_e32 v46, v18
	v_mov_b32_e32 v47, v18
	v_mov_b32_e32 v48, v18
	v_mov_b32_e32 v49, v18
	v_mov_b32_e32 v54, v18
	v_mov_b32_e32 v55, v18
	v_mov_b32_e32 v56, v18
	v_mov_b32_e32 v57, v18
	v_mov_b32_e32 v62, v18
	v_mov_b32_e32 v63, v18
	v_mov_b32_e32 v64, v18
	v_mov_b32_e32 v65, v18
	v_mov_b32_e32 v70, v18
	v_mov_b32_e32 v71, v18
	v_mov_b32_e32 v72, v18
	v_mov_b32_e32 v73, v18
	v_mov_b32_e32 v74, v18
	v_mov_b32_e32 v75, v18
	v_mov_b32_e32 v76, v18
	v_mov_b32_e32 v77, v18
	v_mov_b32_e32 v78, v18
	v_mov_b32_e32 v79, v18
	v_mov_b32_e32 v80, v18
	v_mov_b32_e32 v81, v18
	v_mov_b32_e32 v82, v18
	v_mov_b32_e32 v83, v18
	v_mov_b32_e32 v84, v18
	v_mov_b32_e32 v85, v18
	v_mov_b32_e32 v86, v18
	v_mov_b32_e32 v87, v18
	v_mov_b32_e32 v88, v18
	v_mov_b32_e32 v89, v18
	v_mov_b32_e32 v90, v18
	v_mov_b32_e32 v91, v18
	v_mov_b32_e32 v92, v18
	v_mov_b32_e32 v93, v18
	v_mov_b32_e32 v98, v18
	v_mov_b32_e32 v99, v18
	v_mov_b32_e32 v100, v18
	v_mov_b32_e32 v101, v18
	v_mov_b32_e32 v106, v18
	v_mov_b32_e32 v107, v18
	v_mov_b32_e32 v108, v18
	v_mov_b32_e32 v109, v18
	v_mov_b32_e32 v114, v18
	v_mov_b32_e32 v115, v18
	v_mov_b32_e32 v116, v18
	v_mov_b32_e32 v117, v18
	v_mov_b32_e32 v122, v18
	v_mov_b32_e32 v123, v18
	v_mov_b32_e32 v124, v18
	v_mov_b32_e32 v125, v18
	v_mov_b32_e32 v130, v18
	v_mov_b32_e32 v131, v18
	v_mov_b32_e32 v132, v18
	v_mov_b32_e32 v133, v18
	v_mov_b32_e32 v94, v18
	v_mov_b32_e32 v95, v18
	v_mov_b32_e32 v96, v18
	v_mov_b32_e32 v97, v18
	v_mov_b32_e32 v102, v18
	v_mov_b32_e32 v103, v18
	v_mov_b32_e32 v104, v18
	v_mov_b32_e32 v105, v18
	v_mov_b32_e32 v110, v18
	v_mov_b32_e32 v111, v18
	v_mov_b32_e32 v112, v18
	v_mov_b32_e32 v113, v18
	v_mov_b32_e32 v118, v18
	v_mov_b32_e32 v119, v18
	v_mov_b32_e32 v120, v18
	v_mov_b32_e32 v121, v18
	v_mov_b32_e32 v126, v18
	v_mov_b32_e32 v127, v18
	v_mov_b32_e32 v128, v18
	v_mov_b32_e32 v129, v18
	v_mov_b32_e32 v134, v18
	v_mov_b32_e32 v135, v18
	v_mov_b32_e32 v136, v18
	v_mov_b32_e32 v137, v18
	v_mov_b32_e32 v138, v18
	v_mov_b32_e32 v139, v18
	v_mov_b32_e32 v140, v18
	v_mov_b32_e32 v141, v18
	v_mov_b32_e32 v142, v18
	v_mov_b32_e32 v143, v18
	v_mov_b32_e32 v144, v18
	v_mov_b32_e32 v145, v18
	v_add_u32_e32 v162, 0x18000, v170
	v_add_u32_e32 v163, 0x1c000, v170
.LBB0_202:
	ds_read_b128 v[2:5], v172
	ds_read_b128 v[6:9], v172 offset:1024
	ds_read_b128 v[10:13], v172 offset:2048
	ds_read_b128 v[14:17], v172 offset:3072
	s_add_u32 s34, s30, 0xfffc0080
	s_addc_u32 s35, s31, -1
	s_cmp_eq_u32 s56, 12
	s_cselect_b32 s37, s21, s35
	s_cselect_b32 s36, s52, s34
	s_cselect_b32 s35, s11, s55
	s_cselect_b32 s34, s53, s54
	s_add_i32 m0, s29, 0xc000
	ds_read_b128 v[176:179], v173
	ds_read_b128 v[180:183], v173 offset:1024
	ds_read_b128 v[184:187], v173 offset:2048
	ds_read_b128 v[188:191], v173 offset:3072
	ds_read_b128 v[192:195], v173 offset:4096
	ds_read_b128 v[196:199], v173 offset:5120
	ds_read_b128 v[206:209], v173 offset:6144
	ds_read_b128 v[210:213], v173 offset:7168
	global_load_lds_dwordx4 v154, s[30:31]
	s_add_i32 m0, s29, 0xe000
	s_nop 0
	global_load_lds_dwordx4 v156, s[30:31]
	s_waitcnt lgkmcnt(8)
	s_barrier
	s_waitcnt lgkmcnt(0)
	s_setprio 1
	s_waitcnt lgkmcnt(0)
	v_mfma_scale_f32_16x16x128_f8f6f4 v[142:145], v[2:9], v[176:183], v[142:145], v174, v174 op_sel_hi:[0,0,0]
	v_mfma_scale_f32_16x16x128_f8f6f4 v[138:141], v[10:17], v[176:183], v[138:141], v174, v174 op_sel_hi:[0,0,0]
	v_mfma_scale_f32_16x16x128_f8f6f4 v[134:137], v[2:9], v[184:191], v[134:137], v174, v174 op_sel_hi:[0,0,0]
	v_mfma_scale_f32_16x16x128_f8f6f4 v[126:129], v[10:17], v[184:191], v[126:129], v174, v174 op_sel_hi:[0,0,0]
	v_mfma_scale_f32_16x16x128_f8f6f4 v[118:121], v[2:9], v[192:199], v[118:121], v174, v174 op_sel_hi:[0,0,0]
	v_mfma_scale_f32_16x16x128_f8f6f4 v[110:113], v[10:17], v[192:199], v[110:113], v174, v174 op_sel_hi:[0,0,0]
	v_mfma_scale_f32_16x16x128_f8f6f4 v[102:105], v[2:9], v[206:213], v[102:105], v174, v174 op_sel_hi:[0,0,0]
	v_mfma_scale_f32_16x16x128_f8f6f4 v[94:97], v[10:17], v[206:213], v[94:97], v174, v174 op_sel_hi:[0,0,0]
	s_setprio 0
	s_barrier
	s_add_i32 s57, s48, s38
	s_add_u32 s66, s34, 0x80
	s_addc_u32 s67, s35, 0
	s_mov_b32 m0, s57
	ds_read_b128 v[214:217], v175
	ds_read_b128 v[218:221], v175 offset:1024
	ds_read_b128 v[222:225], v175 offset:2048
	ds_read_b128 v[226:229], v175 offset:3072
	global_load_lds_dwordx4 v150, s[34:35]
	s_add_i32 m0, s57, 0x2000
	s_nop 0
	global_load_lds_dwordx4 v146, s[34:35]
	s_barrier
	s_waitcnt lgkmcnt(0)
	s_setprio 1
	s_waitcnt lgkmcnt(0)
	v_mfma_scale_f32_16x16x128_f8f6f4 v[130:133], v[214:221], v[176:183], v[130:133], v174, v174 op_sel_hi:[0,0,0]
	v_mfma_scale_f32_16x16x128_f8f6f4 v[122:125], v[222:229], v[176:183], v[122:125], v174, v174 op_sel_hi:[0,0,0]
	v_mfma_scale_f32_16x16x128_f8f6f4 v[114:117], v[214:221], v[184:191], v[114:117], v174, v174 op_sel_hi:[0,0,0]
	v_mfma_scale_f32_16x16x128_f8f6f4 v[106:109], v[222:229], v[184:191], v[106:109], v174, v174 op_sel_hi:[0,0,0]
	v_mfma_scale_f32_16x16x128_f8f6f4 v[98:101], v[214:221], v[192:199], v[98:101], v174, v174 op_sel_hi:[0,0,0]
	v_mfma_scale_f32_16x16x128_f8f6f4 v[90:93], v[222:229], v[192:199], v[90:93], v174, v174 op_sel_hi:[0,0,0]
	v_mfma_scale_f32_16x16x128_f8f6f4 v[86:89], v[214:221], v[206:213], v[86:89], v174, v174 op_sel_hi:[0,0,0]
	v_mfma_scale_f32_16x16x128_f8f6f4 v[82:85], v[222:229], v[206:213], v[82:85], v174, v174 op_sel_hi:[0,0,0]
	s_setprio 0
	s_mov_b32 m0, s29
	s_add_u32 s68, s36, 0x80
	s_addc_u32 s69, s37, 0
	s_barrier
	ds_read_b128 v[176:179], v173 offset:16384
	ds_read_b128 v[180:183], v173 offset:17408
	ds_read_b128 v[184:187], v173 offset:18432
	ds_read_b128 v[188:191], v173 offset:19456
	ds_read_b128 v[192:195], v173 offset:20480
	ds_read_b128 v[196:199], v173 offset:21504
	ds_read_b128 v[206:209], v173 offset:22528
	ds_read_b128 v[210:213], v173 offset:23552
	global_load_lds_dwordx4 v152, s[36:37]
	s_mov_b32 m0, s41
	s_nop 0
	global_load_lds_dwordx4 v148, s[36:37]
	s_barrier
	s_waitcnt lgkmcnt(0)
	s_setprio 1
	s_waitcnt lgkmcnt(0)
	v_mfma_scale_f32_16x16x128_f8f6f4 v[78:81], v[2:9], v[176:183], v[78:81], v174, v174 op_sel_hi:[0,0,0]
	v_mfma_scale_f32_16x16x128_f8f6f4 v[74:77], v[10:17], v[176:183], v[74:77], v174, v174 op_sel_hi:[0,0,0]
	v_mfma_scale_f32_16x16x128_f8f6f4 v[70:73], v[2:9], v[184:191], v[70:73], v174, v174 op_sel_hi:[0,0,0]
	v_mfma_scale_f32_16x16x128_f8f6f4 v[62:65], v[10:17], v[184:191], v[62:65], v174, v174 op_sel_hi:[0,0,0]
	v_mfma_scale_f32_16x16x128_f8f6f4 v[54:57], v[2:9], v[192:199], v[54:57], v174, v174 op_sel_hi:[0,0,0]
	v_mfma_scale_f32_16x16x128_f8f6f4 v[46:49], v[10:17], v[192:199], v[46:49], v174, v174 op_sel_hi:[0,0,0]
	v_mfma_scale_f32_16x16x128_f8f6f4 v[38:41], v[2:9], v[206:213], v[38:41], v174, v174 op_sel_hi:[0,0,0]
	v_mfma_scale_f32_16x16x128_f8f6f4 v[30:33], v[10:17], v[206:213], v[30:33], v174, v174 op_sel_hi:[0,0,0]
	s_setprio 0
	s_barrier
	s_add_u32 s60, s34, 0x40000
	s_addc_u32 s61, s35, 0
	s_add_i32 s57, s49, s38
	s_mov_b32 m0, s57
	s_nop 0
	global_load_lds_dwordx4 v150, s[60:61]
	s_add_i32 m0, s57, 0x2000
	s_nop 0
	global_load_lds_dwordx4 v146, s[60:61]
	s_waitcnt vmcnt(6)
	s_barrier
	s_setprio 1
	v_mfma_scale_f32_16x16x128_f8f6f4 v[66:69], v[214:221], v[176:183], v[66:69], v174, v174 op_sel_hi:[0,0,0]
	v_mfma_scale_f32_16x16x128_f8f6f4 v[58:61], v[222:229], v[176:183], v[58:61], v174, v174 op_sel_hi:[0,0,0]
	v_mfma_scale_f32_16x16x128_f8f6f4 v[50:53], v[214:221], v[184:191], v[50:53], v174, v174 op_sel_hi:[0,0,0]
	v_mfma_scale_f32_16x16x128_f8f6f4 v[42:45], v[222:229], v[184:191], v[42:45], v174, v174 op_sel_hi:[0,0,0]
	v_mfma_scale_f32_16x16x128_f8f6f4 v[34:37], v[214:221], v[192:199], v[34:37], v174, v174 op_sel_hi:[0,0,0]
	v_mfma_scale_f32_16x16x128_f8f6f4 v[26:29], v[222:229], v[192:199], v[26:29], v174, v174 op_sel_hi:[0,0,0]
	v_mfma_scale_f32_16x16x128_f8f6f4 v[22:25], v[214:221], v[206:213], v[22:25], v174, v174 op_sel_hi:[0,0,0]
	v_mfma_scale_f32_16x16x128_f8f6f4 v[18:21], v[222:229], v[206:213], v[18:21], v174, v174 op_sel_hi:[0,0,0]
	s_setprio 0
	s_add_i32 s57, 0, 0x18000
	s_barrier
	ds_read_b128 v[2:5], v162
	ds_read_b128 v[6:9], v162 offset:1024
	ds_read_b128 v[10:13], v162 offset:2048
	ds_read_b128 v[14:17], v162 offset:3072
	s_add_u32 s36, s36, 0x40000
	s_addc_u32 s37, s37, 0
	s_mov_b32 m0, s42
	ds_read_b128 v[176:179], v173 offset:32768
	ds_read_b128 v[180:183], v173 offset:33792
	ds_read_b128 v[184:187], v173 offset:34816
	ds_read_b128 v[188:191], v173 offset:35840
	ds_read_b128 v[192:195], v173 offset:36864
	ds_read_b128 v[196:199], v173 offset:37888
	ds_read_b128 v[206:209], v173 offset:38912
	ds_read_b128 v[210:213], v173 offset:39936
	global_load_lds_dwordx4 v152, s[36:37]
	s_mov_b32 m0, s43
	s_nop 0
	global_load_lds_dwordx4 v148, s[36:37]
	s_waitcnt lgkmcnt(8)
	s_barrier
	s_waitcnt lgkmcnt(0)
	s_setprio 1
	s_waitcnt lgkmcnt(0)
	v_mfma_scale_f32_16x16x128_f8f6f4 v[142:145], v[2:9], v[176:183], v[142:145], v174, v174 op_sel_hi:[0,0,0]
	v_mfma_scale_f32_16x16x128_f8f6f4 v[138:141], v[10:17], v[176:183], v[138:141], v174, v174 op_sel_hi:[0,0,0]
	v_mfma_scale_f32_16x16x128_f8f6f4 v[134:137], v[2:9], v[184:191], v[134:137], v174, v174 op_sel_hi:[0,0,0]
	v_mfma_scale_f32_16x16x128_f8f6f4 v[126:129], v[10:17], v[184:191], v[126:129], v174, v174 op_sel_hi:[0,0,0]
	v_mfma_scale_f32_16x16x128_f8f6f4 v[118:121], v[2:9], v[192:199], v[118:121], v174, v174 op_sel_hi:[0,0,0]
	v_mfma_scale_f32_16x16x128_f8f6f4 v[110:113], v[10:17], v[192:199], v[110:113], v174, v174 op_sel_hi:[0,0,0]
	v_mfma_scale_f32_16x16x128_f8f6f4 v[102:105], v[2:9], v[206:213], v[102:105], v174, v174 op_sel_hi:[0,0,0]
	v_mfma_scale_f32_16x16x128_f8f6f4 v[94:97], v[10:17], v[206:213], v[94:97], v174, v174 op_sel_hi:[0,0,0]
	s_setprio 0
	s_barrier
	s_add_i32 s36, 0, 0x1c000
	s_add_i32 s37, s57, s38
	s_mov_b32 m0, s37
	ds_read_b128 v[214:217], v163
	ds_read_b128 v[218:221], v163 offset:1024
	ds_read_b128 v[222:225], v163 offset:2048
	ds_read_b128 v[226:229], v163 offset:3072
	global_load_lds_dwordx4 v150, s[66:67]
	s_add_i32 m0, s37, 0x2000
	s_nop 0
	global_load_lds_dwordx4 v146, s[66:67]
	s_barrier
	s_waitcnt lgkmcnt(0)
	s_setprio 1
	s_waitcnt lgkmcnt(0)
	v_mfma_scale_f32_16x16x128_f8f6f4 v[130:133], v[214:221], v[176:183], v[130:133], v174, v174 op_sel_hi:[0,0,0]
	v_mfma_scale_f32_16x16x128_f8f6f4 v[122:125], v[222:229], v[176:183], v[122:125], v174, v174 op_sel_hi:[0,0,0]
	v_mfma_scale_f32_16x16x128_f8f6f4 v[114:117], v[214:221], v[184:191], v[114:117], v174, v174 op_sel_hi:[0,0,0]
	v_mfma_scale_f32_16x16x128_f8f6f4 v[106:109], v[222:229], v[184:191], v[106:109], v174, v174 op_sel_hi:[0,0,0]
	v_mfma_scale_f32_16x16x128_f8f6f4 v[98:101], v[214:221], v[192:199], v[98:101], v174, v174 op_sel_hi:[0,0,0]
	v_mfma_scale_f32_16x16x128_f8f6f4 v[90:93], v[222:229], v[192:199], v[90:93], v174, v174 op_sel_hi:[0,0,0]
	v_mfma_scale_f32_16x16x128_f8f6f4 v[86:89], v[214:221], v[206:213], v[86:89], v174, v174 op_sel_hi:[0,0,0]
	v_mfma_scale_f32_16x16x128_f8f6f4 v[82:85], v[222:229], v[206:213], v[82:85], v174, v174 op_sel_hi:[0,0,0]
	s_setprio 0
	s_mov_b32 m0, s45
	s_barrier
	ds_read_b128 v[176:179], v173 offset:49152
	ds_read_b128 v[180:183], v173 offset:50176
	ds_read_b128 v[184:187], v173 offset:51200
	ds_read_b128 v[188:191], v173 offset:52224
	ds_read_b128 v[192:195], v173 offset:53248
	ds_read_b128 v[196:199], v173 offset:54272
	ds_read_b128 v[206:209], v173 offset:55296
	ds_read_b128 v[210:213], v173 offset:56320
	global_load_lds_dwordx4 v152, s[68:69]
	s_mov_b32 m0, s46
	s_nop 0
	global_load_lds_dwordx4 v148, s[68:69]
	s_barrier
	s_waitcnt lgkmcnt(0)
	s_setprio 1
	s_waitcnt lgkmcnt(0)
	v_mfma_scale_f32_16x16x128_f8f6f4 v[78:81], v[2:9], v[176:183], v[78:81], v174, v174 op_sel_hi:[0,0,0]
	v_mfma_scale_f32_16x16x128_f8f6f4 v[74:77], v[10:17], v[176:183], v[74:77], v174, v174 op_sel_hi:[0,0,0]
	v_mfma_scale_f32_16x16x128_f8f6f4 v[70:73], v[2:9], v[184:191], v[70:73], v174, v174 op_sel_hi:[0,0,0]
	v_mfma_scale_f32_16x16x128_f8f6f4 v[62:65], v[10:17], v[184:191], v[62:65], v174, v174 op_sel_hi:[0,0,0]
	v_mfma_scale_f32_16x16x128_f8f6f4 v[54:57], v[2:9], v[192:199], v[54:57], v174, v174 op_sel_hi:[0,0,0]
	v_mfma_scale_f32_16x16x128_f8f6f4 v[46:49], v[10:17], v[192:199], v[46:49], v174, v174 op_sel_hi:[0,0,0]
	v_mfma_scale_f32_16x16x128_f8f6f4 v[38:41], v[2:9], v[206:213], v[38:41], v174, v174 op_sel_hi:[0,0,0]
	v_mfma_scale_f32_16x16x128_f8f6f4 v[30:33], v[10:17], v[206:213], v[30:33], v174, v174 op_sel_hi:[0,0,0]
	s_setprio 0
	s_barrier
	s_add_u32 s34, s34, 0x40080
	s_addc_u32 s35, s35, 0
	s_add_i32 s36, s36, s38
	s_mov_b32 m0, s36
	s_nop 0
	global_load_lds_dwordx4 v150, s[34:35]
	s_add_i32 m0, s36, 0x2000
	s_nop 0
	global_load_lds_dwordx4 v146, s[34:35]
	s_waitcnt vmcnt(6)
	s_barrier
	s_setprio 1
	v_mfma_scale_f32_16x16x128_f8f6f4 v[66:69], v[214:221], v[176:183], v[66:69], v174, v174 op_sel_hi:[0,0,0]
	v_mfma_scale_f32_16x16x128_f8f6f4 v[58:61], v[222:229], v[176:183], v[58:61], v174, v174 op_sel_hi:[0,0,0]
	v_mfma_scale_f32_16x16x128_f8f6f4 v[50:53], v[214:221], v[184:191], v[50:53], v174, v174 op_sel_hi:[0,0,0]
	v_mfma_scale_f32_16x16x128_f8f6f4 v[42:45], v[222:229], v[184:191], v[42:45], v174, v174 op_sel_hi:[0,0,0]
	v_mfma_scale_f32_16x16x128_f8f6f4 v[34:37], v[214:221], v[192:199], v[34:37], v174, v174 op_sel_hi:[0,0,0]
	v_mfma_scale_f32_16x16x128_f8f6f4 v[26:29], v[222:229], v[192:199], v[26:29], v174, v174 op_sel_hi:[0,0,0]
	v_mfma_scale_f32_16x16x128_f8f6f4 v[22:25], v[214:221], v[206:213], v[22:25], v174, v174 op_sel_hi:[0,0,0]
	v_mfma_scale_f32_16x16x128_f8f6f4 v[18:21], v[222:229], v[206:213], v[18:21], v174, v174 op_sel_hi:[0,0,0]
	s_setprio 0
	s_add_i32 s56, s56, 2
	s_add_u32 s30, s30, 0x100
	s_addc_u32 s31, s31, 0
	s_add_u32 s54, s54, 0x100
	s_addc_u32 s55, s55, 0
	s_cmp_gt_u32 s56, 13
	s_barrier
	s_cbranch_scc0 .LBB0_202
	v_lshl_or_b32 v4, s51, 8, v171
	v_lshl_add_u32 v16, s28, 8, v1
	v_ashrrev_i32_e32 v5, 31, v4
	v_mov_b64_e32 v[2:3], s[96:97]
	v_mad_i64_i32 v[6:7], s[30:31], v16, s50, v[2:3]
	v_lshlrev_b64 v[4:5], 1, v[4:5]
	v_lshl_add_u64 v[10:11], v[6:7], 0, v[4:5]
	v_pk_mul_f32 v[8:9], v[144:145], s[8:9] op_sel_hi:[1,0]
	v_pk_mul_f32 v[6:7], v[142:143], s[8:9] op_sel_hi:[1,0]
	v_pk_mul_f32 v[12:13], v[140:141], s[8:9] op_sel_hi:[1,0]
	v_pk_mul_f32 v[14:15], v[138:139], s[8:9] op_sel_hi:[1,0]
	v_cvt_pk_bf16_f32 v6, v6, v7
	v_cvt_pk_bf16_f32 v7, v8, v9
	v_cvt_pk_bf16_f32 v8, v14, v15
	v_cvt_pk_bf16_f32 v9, v12, v13
	global_store_dwordx4 v[10:11], v[6:9], off
	v_pk_mul_f32 v[12:13], v[124:125], s[8:9] op_sel_hi:[1,0]
	v_pk_mul_f32 v[14:15], v[122:123], s[8:9] op_sel_hi:[1,0]
	v_pk_mul_f32 v[8:9], v[132:133], s[8:9] op_sel_hi:[1,0]
	v_pk_mul_f32 v[6:7], v[130:131], s[8:9] op_sel_hi:[1,0]
	s_and_b64 vcc, exec, s[0:1]
	v_cvt_pk_bf16_f32 v6, v6, v7
	v_cvt_pk_bf16_f32 v7, v8, v9
	v_cvt_pk_bf16_f32 v8, v14, v15
	v_cvt_pk_bf16_f32 v9, v12, v13
	global_store_dwordx4 v[10:11], v[6:9], off offset:256
	v_pk_mul_f32 v[12:13], v[128:129], s[8:9] op_sel_hi:[1,0]
	v_pk_mul_f32 v[14:15], v[126:127], s[8:9] op_sel_hi:[1,0]
	v_or_b32_e32 v6, 16, v16
	v_mad_i64_i32 v[6:7], s[30:31], v6, s50, v[2:3]
	v_lshl_add_u64 v[10:11], v[6:7], 0, v[4:5]
	v_pk_mul_f32 v[8:9], v[136:137], s[8:9] op_sel_hi:[1,0]
	v_pk_mul_f32 v[6:7], v[134:135], s[8:9] op_sel_hi:[1,0]
	s_mov_b32 s51, s10
	v_cvt_pk_bf16_f32 v6, v6, v7
	v_cvt_pk_bf16_f32 v7, v8, v9
	v_cvt_pk_bf16_f32 v8, v14, v15
	v_cvt_pk_bf16_f32 v9, v12, v13
	global_store_dwordx4 v[10:11], v[6:9], off
	v_pk_mul_f32 v[12:13], v[108:109], s[8:9] op_sel_hi:[1,0]
	v_pk_mul_f32 v[14:15], v[106:107], s[8:9] op_sel_hi:[1,0]
	v_pk_mul_f32 v[8:9], v[116:117], s[8:9] op_sel_hi:[1,0]
	v_pk_mul_f32 v[6:7], v[114:115], s[8:9] op_sel_hi:[1,0]
	s_mov_b32 s28, s20
	v_cvt_pk_bf16_f32 v6, v6, v7
	v_cvt_pk_bf16_f32 v7, v8, v9
	v_cvt_pk_bf16_f32 v8, v14, v15
	v_cvt_pk_bf16_f32 v9, v12, v13
	global_store_dwordx4 v[10:11], v[6:9], off offset:256
	v_pk_mul_f32 v[12:13], v[112:113], s[8:9] op_sel_hi:[1,0]
	v_pk_mul_f32 v[14:15], v[110:111], s[8:9] op_sel_hi:[1,0]
	v_or_b32_e32 v6, 32, v16
	v_mad_i64_i32 v[6:7], s[30:31], v6, s50, v[2:3]
	v_lshl_add_u64 v[10:11], v[6:7], 0, v[4:5]
	v_pk_mul_f32 v[8:9], v[120:121], s[8:9] op_sel_hi:[1,0]
	v_pk_mul_f32 v[6:7], v[118:119], s[8:9] op_sel_hi:[1,0]
	s_mov_b64 s[34:35], s[26:27]
	v_cvt_pk_bf16_f32 v6, v6, v7
	v_cvt_pk_bf16_f32 v7, v8, v9
	v_cvt_pk_bf16_f32 v8, v14, v15
	v_cvt_pk_bf16_f32 v9, v12, v13
	global_store_dwordx4 v[10:11], v[6:9], off
	v_pk_mul_f32 v[12:13], v[92:93], s[8:9] op_sel_hi:[1,0]
	v_pk_mul_f32 v[14:15], v[90:91], s[8:9] op_sel_hi:[1,0]
	v_pk_mul_f32 v[8:9], v[100:101], s[8:9] op_sel_hi:[1,0]
	v_pk_mul_f32 v[6:7], v[98:99], s[8:9] op_sel_hi:[1,0]
	s_nop 0
	v_cvt_pk_bf16_f32 v6, v6, v7
	v_cvt_pk_bf16_f32 v7, v8, v9
	v_cvt_pk_bf16_f32 v8, v14, v15
	v_cvt_pk_bf16_f32 v9, v12, v13
	global_store_dwordx4 v[10:11], v[6:9], off offset:256
	v_pk_mul_f32 v[12:13], v[96:97], s[8:9] op_sel_hi:[1,0]
	v_pk_mul_f32 v[14:15], v[94:95], s[8:9] op_sel_hi:[1,0]
	v_or_b32_e32 v6, 48, v16
	v_mad_i64_i32 v[6:7], s[30:31], v6, s50, v[2:3]
	v_lshl_add_u64 v[10:11], v[6:7], 0, v[4:5]
	v_pk_mul_f32 v[8:9], v[104:105], s[8:9] op_sel_hi:[1,0]
	v_pk_mul_f32 v[6:7], v[102:103], s[8:9] op_sel_hi:[1,0]
	s_nop 0
	v_cvt_pk_bf16_f32 v6, v6, v7
	v_cvt_pk_bf16_f32 v7, v8, v9
	v_cvt_pk_bf16_f32 v8, v14, v15
	v_cvt_pk_bf16_f32 v9, v12, v13
	global_store_dwordx4 v[10:11], v[6:9], off
	v_pk_mul_f32 v[12:13], v[84:85], s[8:9] op_sel_hi:[1,0]
	v_pk_mul_f32 v[14:15], v[82:83], s[8:9] op_sel_hi:[1,0]
	v_pk_mul_f32 v[8:9], v[88:89], s[8:9] op_sel_hi:[1,0]
	v_pk_mul_f32 v[6:7], v[86:87], s[8:9] op_sel_hi:[1,0]
	s_nop 0
	v_cvt_pk_bf16_f32 v6, v6, v7
	v_cvt_pk_bf16_f32 v7, v8, v9
	v_cvt_pk_bf16_f32 v8, v14, v15
	v_cvt_pk_bf16_f32 v9, v12, v13
	global_store_dwordx4 v[10:11], v[6:9], off offset:256
	v_pk_mul_f32 v[12:13], v[76:77], s[8:9] op_sel_hi:[1,0]
	v_pk_mul_f32 v[14:15], v[74:75], s[8:9] op_sel_hi:[1,0]
	v_add_u32_e32 v6, 0x80, v16
	v_mad_i64_i32 v[6:7], s[30:31], v6, s50, v[2:3]
	v_lshl_add_u64 v[10:11], v[6:7], 0, v[4:5]
	v_pk_mul_f32 v[8:9], v[80:81], s[8:9] op_sel_hi:[1,0]
	v_pk_mul_f32 v[6:7], v[78:79], s[8:9] op_sel_hi:[1,0]
	s_nop 0
	v_cvt_pk_bf16_f32 v6, v6, v7
	v_cvt_pk_bf16_f32 v7, v8, v9
	v_cvt_pk_bf16_f32 v8, v14, v15
	v_cvt_pk_bf16_f32 v9, v12, v13
	global_store_dwordx4 v[10:11], v[6:9], off
	v_pk_mul_f32 v[12:13], v[60:61], s[8:9] op_sel_hi:[1,0]
	v_pk_mul_f32 v[14:15], v[58:59], s[8:9] op_sel_hi:[1,0]
	v_pk_mul_f32 v[8:9], v[68:69], s[8:9] op_sel_hi:[1,0]
	v_pk_mul_f32 v[6:7], v[66:67], s[8:9] op_sel_hi:[1,0]
	s_nop 0
	v_cvt_pk_bf16_f32 v6, v6, v7
	v_cvt_pk_bf16_f32 v7, v8, v9
	v_cvt_pk_bf16_f32 v8, v14, v15
	v_cvt_pk_bf16_f32 v9, v12, v13
	global_store_dwordx4 v[10:11], v[6:9], off offset:256
	v_pk_mul_f32 v[12:13], v[64:65], s[8:9] op_sel_hi:[1,0]
	v_pk_mul_f32 v[14:15], v[62:63], s[8:9] op_sel_hi:[1,0]
	v_add_u32_e32 v6, 0x90, v16
	v_mad_i64_i32 v[6:7], s[30:31], v6, s50, v[2:3]
	v_lshl_add_u64 v[10:11], v[6:7], 0, v[4:5]
	v_pk_mul_f32 v[8:9], v[72:73], s[8:9] op_sel_hi:[1,0]
	v_pk_mul_f32 v[6:7], v[70:71], s[8:9] op_sel_hi:[1,0]
	s_nop 0
	v_cvt_pk_bf16_f32 v6, v6, v7
	v_cvt_pk_bf16_f32 v7, v8, v9
	v_cvt_pk_bf16_f32 v8, v14, v15
	v_cvt_pk_bf16_f32 v9, v12, v13
	global_store_dwordx4 v[10:11], v[6:9], off
	v_pk_mul_f32 v[12:13], v[44:45], s[8:9] op_sel_hi:[1,0]
	v_pk_mul_f32 v[14:15], v[42:43], s[8:9] op_sel_hi:[1,0]
	v_pk_mul_f32 v[8:9], v[52:53], s[8:9] op_sel_hi:[1,0]
	v_pk_mul_f32 v[6:7], v[50:51], s[8:9] op_sel_hi:[1,0]
	s_nop 0
	v_cvt_pk_bf16_f32 v6, v6, v7
	v_cvt_pk_bf16_f32 v7, v8, v9
	v_cvt_pk_bf16_f32 v8, v14, v15
	v_cvt_pk_bf16_f32 v9, v12, v13
	global_store_dwordx4 v[10:11], v[6:9], off offset:256
	v_pk_mul_f32 v[12:13], v[48:49], s[8:9] op_sel_hi:[1,0]
	v_pk_mul_f32 v[14:15], v[46:47], s[8:9] op_sel_hi:[1,0]
	v_add_u32_e32 v6, 0xa0, v16
	v_mad_i64_i32 v[6:7], s[30:31], v6, s50, v[2:3]
	v_lshl_add_u64 v[10:11], v[6:7], 0, v[4:5]
	v_pk_mul_f32 v[8:9], v[56:57], s[8:9] op_sel_hi:[1,0]
	v_pk_mul_f32 v[6:7], v[54:55], s[8:9] op_sel_hi:[1,0]
	s_nop 0
	v_cvt_pk_bf16_f32 v6, v6, v7
	v_cvt_pk_bf16_f32 v7, v8, v9
	v_cvt_pk_bf16_f32 v8, v14, v15
	v_cvt_pk_bf16_f32 v9, v12, v13
	global_store_dwordx4 v[10:11], v[6:9], off
	v_pk_mul_f32 v[12:13], v[28:29], s[8:9] op_sel_hi:[1,0]
	v_pk_mul_f32 v[14:15], v[26:27], s[8:9] op_sel_hi:[1,0]
	v_pk_mul_f32 v[8:9], v[36:37], s[8:9] op_sel_hi:[1,0]
	v_pk_mul_f32 v[6:7], v[34:35], s[8:9] op_sel_hi:[1,0]
	s_nop 0
	v_cvt_pk_bf16_f32 v6, v6, v7
	v_cvt_pk_bf16_f32 v7, v8, v9
	v_cvt_pk_bf16_f32 v8, v14, v15
	v_cvt_pk_bf16_f32 v9, v12, v13
	global_store_dwordx4 v[10:11], v[6:9], off offset:256
	v_pk_mul_f32 v[10:11], v[30:31], s[8:9] op_sel_hi:[1,0]
	s_nop 0
	v_add_u32_e32 v6, 0xb0, v16
	v_mad_i64_i32 v[2:3], s[30:31], v6, s50, v[2:3]
	v_lshl_add_u64 v[6:7], v[2:3], 0, v[4:5]
	v_pk_mul_f32 v[4:5], v[40:41], s[8:9] op_sel_hi:[1,0]
	v_pk_mul_f32 v[2:3], v[38:39], s[8:9] op_sel_hi:[1,0]
	v_pk_mul_f32 v[8:9], v[32:33], s[8:9] op_sel_hi:[1,0]
	v_cvt_pk_bf16_f32 v2, v2, v3
	v_cvt_pk_bf16_f32 v3, v4, v5
	v_cvt_pk_bf16_f32 v4, v10, v11
	v_cvt_pk_bf16_f32 v5, v8, v9
	global_store_dwordx4 v[6:7], v[2:5], off
	v_pk_mul_f32 v[8:9], v[20:21], s[8:9] op_sel_hi:[1,0]
	v_pk_mul_f32 v[10:11], v[18:19], s[8:9] op_sel_hi:[1,0]
	v_pk_mul_f32 v[4:5], v[24:25], s[8:9] op_sel_hi:[1,0]
	v_pk_mul_f32 v[2:3], v[22:23], s[8:9] op_sel_hi:[1,0]
	s_mov_b64 s[30:31], s[22:23]
	v_cvt_pk_bf16_f32 v2, v2, v3
	v_cvt_pk_bf16_f32 v3, v4, v5
	v_cvt_pk_bf16_f32 v4, v10, v11
	v_cvt_pk_bf16_f32 v5, v8, v9
	global_store_dwordx4 v[6:7], v[2:5], off offset:256
	s_cbranch_vccz .LBB0_199
	s_waitcnt vmcnt(0)
	s_cmpk_gt_u32 s2, 0xff
	s_cbranch_scc1 .LBB0_206
	s_barrier

.LBB0_619:
	s_ashr_i32 s21, s20, 31
	v_cmp_lt_i64_e32 vcc, s[22:23], v[142:143]
	s_lshl_b64 s[22:23], s[20:21], 20
	v_readlane_b32 s19, v254, 36
	s_add_u32 s22, s19, s22
	v_readlane_b32 s19, v254, 37
	s_addc_u32 s23, s19, s23
	s_and_b64 s[26:27], vcc, exec
	s_cselect_b32 s21, s23, s29
	s_cselect_b32 s54, s22, s28
	s_ashr_i32 s19, s18, 31
	s_lshl_b64 s[26:27], s[18:19], 20
	s_add_u32 s26, s33, s26
	s_addc_u32 s27, s36, s27
	s_and_b64 s[34:35], vcc, exec
	s_cselect_b32 s19, s27, s31
	s_cselect_b32 s55, s26, s30
	s_add_u32 s28, s28, 0x80080
	s_addc_u32 s29, s29, 0
	s_add_u32 s56, s30, 0x100
	v_mov_b32_e32 v2, 0
	s_addc_u32 s57, s31, 0
	s_mov_b32 s60, -2
	v_mov_b32_e32 v3, v2
	v_mov_b32_e32 v4, v2
	v_mov_b32_e32 v5, v2
	v_mov_b32_e32 v6, v2
	v_mov_b32_e32 v7, v2
	v_mov_b32_e32 v8, v2
	v_mov_b32_e32 v9, v2
	v_mov_b32_e32 v10, v2
	v_mov_b32_e32 v11, v2
	v_mov_b32_e32 v12, v2
	v_mov_b32_e32 v13, v2
	v_mov_b32_e32 v14, v2
	v_mov_b32_e32 v15, v2
	v_mov_b32_e32 v16, v2
	v_mov_b32_e32 v17, v2
	v_mov_b32_e32 v26, v2
	v_mov_b32_e32 v27, v2
	v_mov_b32_e32 v28, v2
	v_mov_b32_e32 v29, v2
	v_mov_b32_e32 v30, v2
	v_mov_b32_e32 v31, v2
	v_mov_b32_e32 v32, v2
	v_mov_b32_e32 v33, v2
	v_mov_b32_e32 v42, v2
	v_mov_b32_e32 v43, v2
	v_mov_b32_e32 v44, v2
	v_mov_b32_e32 v45, v2
	v_mov_b32_e32 v46, v2
	v_mov_b32_e32 v47, v2
	v_mov_b32_e32 v48, v2
	v_mov_b32_e32 v49, v2
	v_mov_b32_e32 v18, v2
	v_mov_b32_e32 v19, v2
	v_mov_b32_e32 v20, v2
	v_mov_b32_e32 v21, v2
	v_mov_b32_e32 v22, v2
	v_mov_b32_e32 v23, v2
	v_mov_b32_e32 v24, v2
	v_mov_b32_e32 v25, v2
	v_mov_b32_e32 v34, v2
	v_mov_b32_e32 v35, v2
	v_mov_b32_e32 v36, v2
	v_mov_b32_e32 v37, v2
	v_mov_b32_e32 v38, v2
	v_mov_b32_e32 v39, v2
	v_mov_b32_e32 v40, v2
	v_mov_b32_e32 v41, v2
	v_mov_b32_e32 v50, v2
	v_mov_b32_e32 v51, v2
	v_mov_b32_e32 v52, v2
	v_mov_b32_e32 v53, v2
	v_mov_b32_e32 v54, v2
	v_mov_b32_e32 v55, v2
	v_mov_b32_e32 v56, v2
	v_mov_b32_e32 v57, v2
	v_mov_b32_e32 v58, v2
	v_mov_b32_e32 v59, v2
	v_mov_b32_e32 v60, v2
	v_mov_b32_e32 v61, v2
	v_mov_b32_e32 v62, v2
	v_mov_b32_e32 v63, v2
	v_mov_b32_e32 v64, v2
	v_mov_b32_e32 v65, v2
	v_mov_b32_e32 v66, v2
	v_mov_b32_e32 v67, v2
	v_mov_b32_e32 v68, v2
	v_mov_b32_e32 v69, v2
	v_mov_b32_e32 v70, v2
	v_mov_b32_e32 v71, v2
	v_mov_b32_e32 v72, v2
	v_mov_b32_e32 v73, v2
	v_mov_b32_e32 v74, v2
	v_mov_b32_e32 v75, v2
	v_mov_b32_e32 v76, v2
	v_mov_b32_e32 v77, v2
	v_mov_b32_e32 v78, v2
	v_mov_b32_e32 v79, v2
	v_mov_b32_e32 v80, v2
	v_mov_b32_e32 v81, v2
	v_mov_b32_e32 v90, v2
	v_mov_b32_e32 v91, v2
	v_mov_b32_e32 v92, v2
	v_mov_b32_e32 v93, v2
	v_mov_b32_e32 v94, v2
	v_mov_b32_e32 v95, v2
	v_mov_b32_e32 v96, v2
	v_mov_b32_e32 v97, v2
	v_mov_b32_e32 v106, v2
	v_mov_b32_e32 v107, v2
	v_mov_b32_e32 v108, v2
	v_mov_b32_e32 v109, v2
	v_mov_b32_e32 v110, v2
	v_mov_b32_e32 v111, v2
	v_mov_b32_e32 v112, v2
	v_mov_b32_e32 v113, v2
	v_mov_b32_e32 v82, v2
	v_mov_b32_e32 v83, v2
	v_mov_b32_e32 v84, v2
	v_mov_b32_e32 v85, v2
	v_mov_b32_e32 v86, v2
	v_mov_b32_e32 v87, v2
	v_mov_b32_e32 v88, v2
	v_mov_b32_e32 v89, v2
	v_mov_b32_e32 v98, v2
	v_mov_b32_e32 v99, v2
	v_mov_b32_e32 v100, v2
	v_mov_b32_e32 v101, v2
	v_mov_b32_e32 v102, v2
	v_mov_b32_e32 v103, v2
	v_mov_b32_e32 v104, v2
	v_mov_b32_e32 v105, v2
	v_mov_b32_e32 v114, v2
	v_mov_b32_e32 v115, v2
	v_mov_b32_e32 v116, v2
	v_mov_b32_e32 v117, v2
	v_mov_b32_e32 v118, v2
	v_mov_b32_e32 v119, v2
	v_mov_b32_e32 v120, v2
	v_mov_b32_e32 v121, v2
	v_mov_b32_e32 v122, v2
	v_mov_b32_e32 v123, v2
	v_mov_b32_e32 v124, v2
	v_mov_b32_e32 v125, v2
	v_mov_b32_e32 v126, v2
	v_mov_b32_e32 v127, v2
	v_mov_b32_e32 v128, v2
	v_mov_b32_e32 v129, v2
	v_add_u32_e32 v232, 0x18000, v146
	v_add_u32_e32 v233, 0x1c000, v146
.LBB0_620:
	ds_read_b128 v[152:155], v148
	ds_read_b128 v[156:159], v148 offset:1024
	ds_read_b128 v[160:163], v148 offset:2048
	ds_read_b128 v[164:167], v148 offset:3072
	s_add_u32 s30, s28, 0xfff80080
	s_addc_u32 s31, s29, -1
	s_cmp_eq_u32 s60, 28
	s_cselect_b32 s35, s21, s31
	s_cselect_b32 s34, s54, s30
	s_cselect_b32 s31, s19, s57
	s_cselect_b32 s30, s55, s56
	s_add_i32 m0, s17, 0xc000
	ds_read_b128 v[168:171], v149
	ds_read_b128 v[172:175], v149 offset:1024
	ds_read_b128 v[176:179], v149 offset:2048
	ds_read_b128 v[180:183], v149 offset:3072
	ds_read_b128 v[184:187], v149 offset:4096
	ds_read_b128 v[188:191], v149 offset:5120
	ds_read_b128 v[192:195], v149 offset:6144
	ds_read_b128 v[196:199], v149 offset:7168
	global_load_lds_dwordx4 v138, s[28:29]
	s_add_i32 m0, s17, 0xe000
	s_nop 0
	global_load_lds_dwordx4 v140, s[28:29]
	s_waitcnt lgkmcnt(8)
	s_barrier
	s_waitcnt lgkmcnt(0)
	s_setprio 1
	s_waitcnt lgkmcnt(0)
	v_mfma_f32_16x16x32_bf16 v[126:129], v[152:155], v[168:171], v[126:129]
	v_mfma_f32_16x16x32_bf16 v[122:125], v[160:163], v[168:171], v[122:125]
	v_mfma_f32_16x16x32_bf16 v[118:121], v[152:155], v[176:179], v[118:121]
	v_mfma_f32_16x16x32_bf16 v[114:117], v[160:163], v[176:179], v[114:117]
	v_mfma_f32_16x16x32_bf16 v[102:105], v[152:155], v[184:187], v[102:105]
	v_mfma_f32_16x16x32_bf16 v[98:101], v[160:163], v[184:187], v[98:101]
	v_mfma_f32_16x16x32_bf16 v[86:89], v[152:155], v[192:195], v[86:89]
	v_mfma_f32_16x16x32_bf16 v[82:85], v[160:163], v[192:195], v[82:85]
	v_mfma_f32_16x16x32_bf16 v[126:129], v[156:159], v[172:175], v[126:129]
	v_mfma_f32_16x16x32_bf16 v[122:125], v[164:167], v[172:175], v[122:125]
	v_mfma_f32_16x16x32_bf16 v[118:121], v[156:159], v[180:183], v[118:121]
	v_mfma_f32_16x16x32_bf16 v[114:117], v[164:167], v[180:183], v[114:117]
	v_mfma_f32_16x16x32_bf16 v[102:105], v[156:159], v[188:191], v[102:105]
	v_mfma_f32_16x16x32_bf16 v[98:101], v[164:167], v[188:191], v[98:101]
	v_mfma_f32_16x16x32_bf16 v[86:89], v[156:159], v[196:199], v[86:89]
	v_mfma_f32_16x16x32_bf16 v[82:85], v[164:167], v[196:199], v[82:85]
	s_setprio 0
	s_barrier
	s_add_i32 s61, s47, s37
	s_add_u32 s66, s30, 0x80
	s_addc_u32 s67, s31, 0
	s_mov_b32 m0, s61
	ds_read_b128 v[200:203], v150
	ds_read_b128 v[206:209], v150 offset:1024
	ds_read_b128 v[210:213], v150 offset:2048
	ds_read_b128 v[214:217], v150 offset:3072
	global_load_lds_dwordx4 v134, s[30:31]
	s_add_i32 m0, s61, 0x2000
	s_nop 0
	global_load_lds_dwordx4 v130, s[30:31]
	s_barrier
	s_waitcnt lgkmcnt(0)
	s_setprio 1
	s_waitcnt lgkmcnt(0)
	v_mfma_f32_16x16x32_bf16 v[110:113], v[200:203], v[168:171], v[110:113]
	v_mfma_f32_16x16x32_bf16 v[106:109], v[210:213], v[168:171], v[106:109]
	v_mfma_f32_16x16x32_bf16 v[94:97], v[200:203], v[176:179], v[94:97]
	v_mfma_f32_16x16x32_bf16 v[90:93], v[210:213], v[176:179], v[90:93]
	v_mfma_f32_16x16x32_bf16 v[78:81], v[200:203], v[184:187], v[78:81]
	v_mfma_f32_16x16x32_bf16 v[74:77], v[210:213], v[184:187], v[74:77]
	v_mfma_f32_16x16x32_bf16 v[70:73], v[200:203], v[192:195], v[70:73]
	v_mfma_f32_16x16x32_bf16 v[66:69], v[210:213], v[192:195], v[66:69]
	v_mfma_f32_16x16x32_bf16 v[110:113], v[206:209], v[172:175], v[110:113]
	v_mfma_f32_16x16x32_bf16 v[106:109], v[214:217], v[172:175], v[106:109]
	v_mfma_f32_16x16x32_bf16 v[94:97], v[206:209], v[180:183], v[94:97]
	v_mfma_f32_16x16x32_bf16 v[90:93], v[214:217], v[180:183], v[90:93]
	v_mfma_f32_16x16x32_bf16 v[78:81], v[206:209], v[188:191], v[78:81]
	v_mfma_f32_16x16x32_bf16 v[74:77], v[214:217], v[188:191], v[74:77]
	v_mfma_f32_16x16x32_bf16 v[70:73], v[206:209], v[196:199], v[70:73]
	v_mfma_f32_16x16x32_bf16 v[66:69], v[214:217], v[196:199], v[66:69]
	s_setprio 0
	s_mov_b32 m0, s17
	s_add_u32 s68, s34, 0x80
	s_addc_u32 s69, s35, 0
	s_barrier
	ds_read_b128 v[168:171], v149 offset:16384
	ds_read_b128 v[172:175], v149 offset:17408
	ds_read_b128 v[176:179], v149 offset:18432
	ds_read_b128 v[180:183], v149 offset:19456
	ds_read_b128 v[184:187], v149 offset:20480
	ds_read_b128 v[188:191], v149 offset:21504
	ds_read_b128 v[192:195], v149 offset:22528
	ds_read_b128 v[196:199], v149 offset:23552
	global_load_lds_dwordx4 v136, s[34:35]
	s_mov_b32 m0, s40
	s_nop 0
	global_load_lds_dwordx4 v132, s[34:35]
	s_barrier
	s_waitcnt lgkmcnt(0)
	s_setprio 1
	s_waitcnt lgkmcnt(0)
	v_mfma_f32_16x16x32_bf16 v[62:65], v[152:155], v[168:171], v[62:65]
	v_mfma_f32_16x16x32_bf16 v[58:61], v[160:163], v[168:171], v[58:61]
	v_mfma_f32_16x16x32_bf16 v[54:57], v[152:155], v[176:179], v[54:57]
	v_mfma_f32_16x16x32_bf16 v[50:53], v[160:163], v[176:179], v[50:53]
	v_mfma_f32_16x16x32_bf16 v[38:41], v[152:155], v[184:187], v[38:41]
	v_mfma_f32_16x16x32_bf16 v[34:37], v[160:163], v[184:187], v[34:37]
	v_mfma_f32_16x16x32_bf16 v[22:25], v[152:155], v[192:195], v[22:25]
	v_mfma_f32_16x16x32_bf16 v[18:21], v[160:163], v[192:195], v[18:21]
	v_mfma_f32_16x16x32_bf16 v[62:65], v[156:159], v[172:175], v[62:65]
	v_mfma_f32_16x16x32_bf16 v[58:61], v[164:167], v[172:175], v[58:61]
	v_mfma_f32_16x16x32_bf16 v[54:57], v[156:159], v[180:183], v[54:57]
	v_mfma_f32_16x16x32_bf16 v[50:53], v[164:167], v[180:183], v[50:53]
	v_mfma_f32_16x16x32_bf16 v[38:41], v[156:159], v[188:191], v[38:41]
	v_mfma_f32_16x16x32_bf16 v[34:37], v[164:167], v[188:191], v[34:37]
	v_mfma_f32_16x16x32_bf16 v[22:25], v[156:159], v[196:199], v[22:25]
	v_mfma_f32_16x16x32_bf16 v[18:21], v[164:167], v[196:199], v[18:21]
	s_setprio 0
	s_barrier
	s_add_u32 s62, s30, 0x80000
	s_addc_u32 s63, s31, 0
	s_add_i32 s61, s48, s37
	s_mov_b32 m0, s61
	s_nop 0
	global_load_lds_dwordx4 v134, s[62:63]
	s_add_i32 m0, s61, 0x2000
	s_nop 0
	global_load_lds_dwordx4 v130, s[62:63]
	s_waitcnt vmcnt(6)
	s_barrier
	s_setprio 1
	v_mfma_f32_16x16x32_bf16 v[46:49], v[200:203], v[168:171], v[46:49]
	v_mfma_f32_16x16x32_bf16 v[42:45], v[210:213], v[168:171], v[42:45]
	v_mfma_f32_16x16x32_bf16 v[30:33], v[200:203], v[176:179], v[30:33]
	v_mfma_f32_16x16x32_bf16 v[26:29], v[210:213], v[176:179], v[26:29]
	v_mfma_f32_16x16x32_bf16 v[14:17], v[200:203], v[184:187], v[14:17]
	v_mfma_f32_16x16x32_bf16 v[10:13], v[210:213], v[184:187], v[10:13]
	v_mfma_f32_16x16x32_bf16 v[6:9], v[200:203], v[192:195], v[6:9]
	v_mfma_f32_16x16x32_bf16 v[2:5], v[210:213], v[192:195], v[2:5]
	v_mfma_f32_16x16x32_bf16 v[46:49], v[206:209], v[172:175], v[46:49]
	v_mfma_f32_16x16x32_bf16 v[42:45], v[214:217], v[172:175], v[42:45]
	v_mfma_f32_16x16x32_bf16 v[30:33], v[206:209], v[180:183], v[30:33]
	v_mfma_f32_16x16x32_bf16 v[26:29], v[214:217], v[180:183], v[26:29]
	v_mfma_f32_16x16x32_bf16 v[14:17], v[206:209], v[188:191], v[14:17]
	v_mfma_f32_16x16x32_bf16 v[10:13], v[214:217], v[188:191], v[10:13]
	v_mfma_f32_16x16x32_bf16 v[6:9], v[206:209], v[196:199], v[6:9]
	v_mfma_f32_16x16x32_bf16 v[2:5], v[214:217], v[196:199], v[2:5]
	s_setprio 0
	s_add_i32 s61, 0, 0x18000
	s_barrier
	ds_read_b128 v[152:155], v232
	ds_read_b128 v[156:159], v232 offset:1024
	ds_read_b128 v[160:163], v232 offset:2048
	ds_read_b128 v[164:167], v232 offset:3072
	s_add_u32 s34, s34, 0x80000
	s_addc_u32 s35, s35, 0
	s_mov_b32 m0, s41
	ds_read_b128 v[168:171], v149 offset:32768
	ds_read_b128 v[172:175], v149 offset:33792
	ds_read_b128 v[176:179], v149 offset:34816
	ds_read_b128 v[180:183], v149 offset:35840
	ds_read_b128 v[184:187], v149 offset:36864
	ds_read_b128 v[188:191], v149 offset:37888
	ds_read_b128 v[192:195], v149 offset:38912
	ds_read_b128 v[196:199], v149 offset:39936
	global_load_lds_dwordx4 v136, s[34:35]
	s_mov_b32 m0, s42
	s_nop 0
	global_load_lds_dwordx4 v132, s[34:35]
	s_waitcnt lgkmcnt(8)
	s_barrier
	s_waitcnt lgkmcnt(0)
	s_setprio 1
	s_waitcnt lgkmcnt(0)
	v_mfma_f32_16x16x32_bf16 v[126:129], v[152:155], v[168:171], v[126:129]
	v_mfma_f32_16x16x32_bf16 v[122:125], v[160:163], v[168:171], v[122:125]
	v_mfma_f32_16x16x32_bf16 v[118:121], v[152:155], v[176:179], v[118:121]
	v_mfma_f32_16x16x32_bf16 v[114:117], v[160:163], v[176:179], v[114:117]
	v_mfma_f32_16x16x32_bf16 v[102:105], v[152:155], v[184:187], v[102:105]
	v_mfma_f32_16x16x32_bf16 v[98:101], v[160:163], v[184:187], v[98:101]
	v_mfma_f32_16x16x32_bf16 v[86:89], v[152:155], v[192:195], v[86:89]
	v_mfma_f32_16x16x32_bf16 v[82:85], v[160:163], v[192:195], v[82:85]
	v_mfma_f32_16x16x32_bf16 v[126:129], v[156:159], v[172:175], v[126:129]
	v_mfma_f32_16x16x32_bf16 v[122:125], v[164:167], v[172:175], v[122:125]
	v_mfma_f32_16x16x32_bf16 v[118:121], v[156:159], v[180:183], v[118:121]
	v_mfma_f32_16x16x32_bf16 v[114:117], v[164:167], v[180:183], v[114:117]
	v_mfma_f32_16x16x32_bf16 v[102:105], v[156:159], v[188:191], v[102:105]
	v_mfma_f32_16x16x32_bf16 v[98:101], v[164:167], v[188:191], v[98:101]
	v_mfma_f32_16x16x32_bf16 v[86:89], v[156:159], v[196:199], v[86:89]
	v_mfma_f32_16x16x32_bf16 v[82:85], v[164:167], v[196:199], v[82:85]
	s_setprio 0
	s_barrier
	s_add_i32 s34, 0, 0x1c000
	s_add_i32 s35, s61, s37
	s_mov_b32 m0, s35
	ds_read_b128 v[200:203], v233
	ds_read_b128 v[206:209], v233 offset:1024
	ds_read_b128 v[210:213], v233 offset:2048
	ds_read_b128 v[214:217], v233 offset:3072
	global_load_lds_dwordx4 v134, s[66:67]
	s_add_i32 m0, s35, 0x2000
	s_nop 0
	global_load_lds_dwordx4 v130, s[66:67]
	s_barrier
	s_waitcnt lgkmcnt(0)
	s_setprio 1
	s_waitcnt lgkmcnt(0)
	v_mfma_f32_16x16x32_bf16 v[110:113], v[200:203], v[168:171], v[110:113]
	v_mfma_f32_16x16x32_bf16 v[106:109], v[210:213], v[168:171], v[106:109]
	v_mfma_f32_16x16x32_bf16 v[94:97], v[200:203], v[176:179], v[94:97]
	v_mfma_f32_16x16x32_bf16 v[90:93], v[210:213], v[176:179], v[90:93]
	v_mfma_f32_16x16x32_bf16 v[78:81], v[200:203], v[184:187], v[78:81]
	v_mfma_f32_16x16x32_bf16 v[74:77], v[210:213], v[184:187], v[74:77]
	v_mfma_f32_16x16x32_bf16 v[70:73], v[200:203], v[192:195], v[70:73]
	v_mfma_f32_16x16x32_bf16 v[66:69], v[210:213], v[192:195], v[66:69]
	v_mfma_f32_16x16x32_bf16 v[110:113], v[206:209], v[172:175], v[110:113]
	v_mfma_f32_16x16x32_bf16 v[106:109], v[214:217], v[172:175], v[106:109]
	v_mfma_f32_16x16x32_bf16 v[94:97], v[206:209], v[180:183], v[94:97]
	v_mfma_f32_16x16x32_bf16 v[90:93], v[214:217], v[180:183], v[90:93]
	v_mfma_f32_16x16x32_bf16 v[78:81], v[206:209], v[188:191], v[78:81]
	v_mfma_f32_16x16x32_bf16 v[74:77], v[214:217], v[188:191], v[74:77]
	v_mfma_f32_16x16x32_bf16 v[70:73], v[206:209], v[196:199], v[70:73]
	v_mfma_f32_16x16x32_bf16 v[66:69], v[214:217], v[196:199], v[66:69]
	s_setprio 0
	s_mov_b32 m0, s44
	s_barrier
	ds_read_b128 v[168:171], v149 offset:49152
	ds_read_b128 v[172:175], v149 offset:50176
	ds_read_b128 v[176:179], v149 offset:51200
	ds_read_b128 v[180:183], v149 offset:52224
	ds_read_b128 v[184:187], v149 offset:53248
	ds_read_b128 v[188:191], v149 offset:54272
	ds_read_b128 v[192:195], v149 offset:55296
	ds_read_b128 v[196:199], v149 offset:56320
	global_load_lds_dwordx4 v136, s[68:69]
	s_mov_b32 m0, s45
	s_nop 0
	global_load_lds_dwordx4 v132, s[68:69]
	s_barrier
	s_waitcnt lgkmcnt(0)
	s_setprio 1
	s_waitcnt lgkmcnt(0)
	v_mfma_f32_16x16x32_bf16 v[62:65], v[152:155], v[168:171], v[62:65]
	v_mfma_f32_16x16x32_bf16 v[58:61], v[160:163], v[168:171], v[58:61]
	v_mfma_f32_16x16x32_bf16 v[54:57], v[152:155], v[176:179], v[54:57]
	v_mfma_f32_16x16x32_bf16 v[50:53], v[160:163], v[176:179], v[50:53]
	v_mfma_f32_16x16x32_bf16 v[38:41], v[152:155], v[184:187], v[38:41]
	v_mfma_f32_16x16x32_bf16 v[34:37], v[160:163], v[184:187], v[34:37]
	v_mfma_f32_16x16x32_bf16 v[22:25], v[152:155], v[192:195], v[22:25]
	v_mfma_f32_16x16x32_bf16 v[18:21], v[160:163], v[192:195], v[18:21]
	v_mfma_f32_16x16x32_bf16 v[62:65], v[156:159], v[172:175], v[62:65]
	v_mfma_f32_16x16x32_bf16 v[58:61], v[164:167], v[172:175], v[58:61]
	v_mfma_f32_16x16x32_bf16 v[54:57], v[156:159], v[180:183], v[54:57]
	v_mfma_f32_16x16x32_bf16 v[50:53], v[164:167], v[180:183], v[50:53]
	v_mfma_f32_16x16x32_bf16 v[38:41], v[156:159], v[188:191], v[38:41]
	v_mfma_f32_16x16x32_bf16 v[34:37], v[164:167], v[188:191], v[34:37]
	v_mfma_f32_16x16x32_bf16 v[22:25], v[156:159], v[196:199], v[22:25]
	v_mfma_f32_16x16x32_bf16 v[18:21], v[164:167], v[196:199], v[18:21]
	s_setprio 0
	s_barrier
	s_add_u32 s30, s30, 0x80080
	s_addc_u32 s31, s31, 0
	s_add_i32 s34, s34, s37
	s_mov_b32 m0, s34
	s_nop 0
	global_load_lds_dwordx4 v134, s[30:31]
	s_add_i32 m0, s34, 0x2000
	s_nop 0
	global_load_lds_dwordx4 v130, s[30:31]
	s_waitcnt vmcnt(6)
	s_barrier
	s_setprio 1
	v_mfma_f32_16x16x32_bf16 v[46:49], v[200:203], v[168:171], v[46:49]
	v_mfma_f32_16x16x32_bf16 v[42:45], v[210:213], v[168:171], v[42:45]
	v_mfma_f32_16x16x32_bf16 v[30:33], v[200:203], v[176:179], v[30:33]
	v_mfma_f32_16x16x32_bf16 v[26:29], v[210:213], v[176:179], v[26:29]
	v_mfma_f32_16x16x32_bf16 v[14:17], v[200:203], v[184:187], v[14:17]
	v_mfma_f32_16x16x32_bf16 v[10:13], v[210:213], v[184:187], v[10:13]
	v_mfma_f32_16x16x32_bf16 v[6:9], v[200:203], v[192:195], v[6:9]
	v_mfma_f32_16x16x32_bf16 v[2:5], v[210:213], v[192:195], v[2:5]
	v_mfma_f32_16x16x32_bf16 v[46:49], v[206:209], v[172:175], v[46:49]
	v_mfma_f32_16x16x32_bf16 v[42:45], v[214:217], v[172:175], v[42:45]
	v_mfma_f32_16x16x32_bf16 v[30:33], v[206:209], v[180:183], v[30:33]
	v_mfma_f32_16x16x32_bf16 v[26:29], v[214:217], v[180:183], v[26:29]
	v_mfma_f32_16x16x32_bf16 v[14:17], v[206:209], v[188:191], v[14:17]
	v_mfma_f32_16x16x32_bf16 v[10:13], v[214:217], v[188:191], v[10:13]
	v_mfma_f32_16x16x32_bf16 v[6:9], v[206:209], v[196:199], v[6:9]
	v_mfma_f32_16x16x32_bf16 v[2:5], v[214:217], v[196:199], v[2:5]
	s_setprio 0
	s_add_i32 s60, s60, 2
	s_add_u32 s28, s28, 0x100
	s_addc_u32 s29, s29, 0
	s_add_u32 s56, s56, 0x100
	s_addc_u32 s57, s57, 0
	s_cmp_gt_u32 s60, 29
	s_barrier
	s_cbranch_scc0 .LBB0_620
	v_lshl_add_u32 v152, s16, 8, v1
	v_lshl_or_b32 v154, s53, 8, v147
	v_ashrrev_i32_e32 v153, 31, v152
	v_ashrrev_i32_e32 v155, 31, v154
	v_lshlrev_b64 v[156:157], 12, v[152:153]
	v_lshl_add_u64 v[156:157], s[96:97], 0, v[156:157]
	v_lshlrev_b64 v[154:155], 1, v[154:155]
	v_lshl_add_u64 v[156:157], v[156:157], 0, v[154:155]
	v_cvt_pk_bf16_f32 v62, v62, v63
	v_cvt_pk_bf16_f32 v63, v64, v65
	v_cvt_pk_bf16_f32 v64, v58, v59
	v_add_co_u32_e32 v58, vcc, s49, v156
	v_cvt_pk_bf16_f32 v70, v70, v71
	v_cvt_pk_bf16_f32 v71, v72, v73
	v_cvt_pk_bf16_f32 v72, v66, v67
	v_lshl_add_u64 v[66:67], v[156:157], 0, s[6:7]
	v_addc_co_u32_e32 v59, vcc, 0, v157, vcc
	v_cvt_pk_bf16_f32 v46, v46, v47
	v_cvt_pk_bf16_f32 v47, v48, v49
	v_cvt_pk_bf16_f32 v48, v42, v43
	v_cvt_pk_bf16_f32 v49, v44, v45
	v_cvt_pk_bf16_f32 v110, v110, v111
	v_cvt_pk_bf16_f32 v111, v112, v113
	v_cvt_pk_bf16_f32 v112, v106, v107
	v_or_b32_e32 v106, 16, v152
	global_store_dwordx4 v[66:67], v[46:49], off offset:256
	v_ashrrev_i32_e32 v107, 31, v106
	v_cvt_pk_bf16_f32 v94, v94, v95
	v_add_co_u32_e32 v48, vcc, s50, v156
	v_cvt_pk_bf16_f32 v95, v96, v97
	v_cvt_pk_bf16_f32 v96, v90, v91
	v_or_b32_e32 v90, 32, v152
	v_lshl_add_u64 v[46:47], v[156:157], 0, s[10:11]
	v_addc_co_u32_e32 v49, vcc, 0, v157, vcc
	v_cvt_pk_bf16_f32 v30, v30, v31
	v_cvt_pk_bf16_f32 v31, v32, v33
	v_cvt_pk_bf16_f32 v32, v26, v27
	v_cvt_pk_bf16_f32 v33, v28, v29
	v_lshlrev_b64 v[106:107], 12, v[106:107]
	v_ashrrev_i32_e32 v91, 31, v90
	v_cvt_pk_bf16_f32 v78, v78, v79
	v_cvt_pk_bf16_f32 v79, v80, v81
	v_cvt_pk_bf16_f32 v80, v74, v75
	v_or_b32_e32 v74, 48, v152
	global_store_dwordx4 v[46:47], v[30:33], off offset:256
	v_cvt_pk_bf16_f32 v113, v108, v109
	v_lshl_add_u64 v[106:107], s[96:97], 0, v[106:107]
	v_add_co_u32_e32 v32, vcc, s51, v156
	v_lshlrev_b64 v[90:91], 12, v[90:91]
	v_ashrrev_i32_e32 v75, 31, v74
	v_lshl_add_u64 v[30:31], v[156:157], 0, s[12:13]
	v_addc_co_u32_e32 v33, vcc, 0, v157, vcc
	v_cvt_pk_bf16_f32 v14, v14, v15
	v_cvt_pk_bf16_f32 v15, v16, v17
	v_cvt_pk_bf16_f32 v16, v10, v11
	v_cvt_pk_bf16_f32 v17, v12, v13
	global_store_dwordx4 v[156:157], v[110:113], off offset:256
	v_cvt_pk_bf16_f32 v97, v92, v93
	v_lshl_add_u64 v[90:91], s[96:97], 0, v[90:91]
	v_lshl_add_u64 v[110:111], v[106:107], 0, v[154:155]
	v_lshlrev_b64 v[74:75], 12, v[74:75]
	global_store_dwordx4 v[30:31], v[14:17], off offset:256
	global_store_dwordx4 v[110:111], v[94:97], off offset:256
	v_cvt_pk_bf16_f32 v81, v76, v77
	v_add_co_u32_e32 v16, vcc, s52, v156
	v_lshl_add_u64 v[94:95], v[90:91], 0, v[154:155]
	v_lshl_add_u64 v[74:75], s[96:97], 0, v[74:75]
	v_addc_co_u32_e32 v17, vcc, 0, v157, vcc
	v_cvt_pk_bf16_f32 v126, v126, v127
	v_cvt_pk_bf16_f32 v127, v128, v129
	v_cvt_pk_bf16_f32 v128, v122, v123
	v_cvt_pk_bf16_f32 v129, v124, v125
	v_cvt_pk_bf16_f32 v106, v118, v119
	v_cvt_pk_bf16_f32 v107, v120, v121
	v_cvt_pk_bf16_f32 v108, v114, v115
	v_cvt_pk_bf16_f32 v109, v116, v117
	v_cvt_pk_bf16_f32 v90, v102, v103
	v_cvt_pk_bf16_f32 v91, v104, v105
	v_cvt_pk_bf16_f32 v92, v98, v99
	v_cvt_pk_bf16_f32 v93, v100, v101
	global_store_dwordx4 v[94:95], v[78:81], off offset:256
	v_cvt_pk_bf16_f32 v76, v82, v83
	v_cvt_pk_bf16_f32 v77, v84, v85
	v_lshl_add_u64 v[78:79], v[74:75], 0, v[154:155]
	v_cvt_pk_bf16_f32 v74, v86, v87
	v_cvt_pk_bf16_f32 v75, v88, v89
	v_cvt_pk_bf16_f32 v73, v68, v69
	v_cvt_pk_bf16_f32 v65, v60, v61
	v_cvt_pk_bf16_f32 v42, v54, v55
	v_cvt_pk_bf16_f32 v43, v56, v57
	v_cvt_pk_bf16_f32 v44, v50, v51
	v_cvt_pk_bf16_f32 v45, v52, v53
	v_cvt_pk_bf16_f32 v26, v38, v39
	v_cvt_pk_bf16_f32 v27, v40, v41
	v_cvt_pk_bf16_f32 v28, v34, v35
	v_cvt_pk_bf16_f32 v29, v36, v37
	v_lshl_add_u64 v[14:15], v[156:157], 0, s[14:15]
	v_cvt_pk_bf16_f32 v10, v22, v23
	v_cvt_pk_bf16_f32 v11, v24, v25
	v_cvt_pk_bf16_f32 v12, v18, v19
	v_cvt_pk_bf16_f32 v13, v20, v21
	v_cvt_pk_bf16_f32 v6, v6, v7
	v_cvt_pk_bf16_f32 v7, v8, v9
	v_cvt_pk_bf16_f32 v8, v2, v3
	v_cvt_pk_bf16_f32 v9, v4, v5
	s_and_b64 vcc, exec, s[0:1]
	s_mov_b32 s53, s18
	s_mov_b32 s16, s20
	s_mov_b64 s[30:31], s[26:27]
	s_mov_b64 s[28:29], s[22:23]
	global_store_dwordx4 v[156:157], v[126:129], off
	global_store_dwordx4 v[110:111], v[106:109], off
	global_store_dwordx4 v[94:95], v[90:93], off
	global_store_dwordx4 v[78:79], v[74:77], off
	global_store_dwordx4 v[78:79], v[70:73], off offset:256
	global_store_dwordx4 v[58:59], v[62:65], off
	global_store_dwordx4 v[48:49], v[42:45], off
	global_store_dwordx4 v[32:33], v[26:29], off
	global_store_dwordx4 v[16:17], v[10:13], off
	global_store_dwordx4 v[14:15], v[6:9], off offset:256
	s_cbranch_vccz .LBB0_617
	s_waitcnt vmcnt(0)
	s_cmpk_gt_u32 s2, 0xff
	s_cbranch_scc1 .LBB0_624
	s_barrier

.LBB0_1368:
	s_ashr_i32 s21, s20, 31
	v_cmp_lt_i64_e32 vcc, s[22:23], v[142:143]
	s_lshl_b64 s[22:23], s[20:21], 20
	v_readlane_b32 s19, v254, 36
	s_add_u32 s22, s19, s22
	v_readlane_b32 s19, v254, 37
	s_addc_u32 s23, s19, s23
	s_and_b64 s[24:25], vcc, exec
	s_cselect_b32 s21, s23, s27
	s_cselect_b32 s50, s22, s26
	s_ashr_i32 s19, s18, 31
	s_lshl_b64 s[24:25], s[18:19], 20
	s_add_u32 s24, s33, s24
	s_addc_u32 s25, s34, s25
	s_and_b64 s[30:31], vcc, exec
	s_cselect_b32 s19, s25, s29
	s_cselect_b32 s51, s24, s28
	s_add_u32 s26, s26, 0x80080
	s_addc_u32 s27, s27, 0
	s_add_u32 s52, s28, 0x100
	v_mov_b32_e32 v2, 0
	s_addc_u32 s53, s29, 0
	s_mov_b32 s54, -2
	v_mov_b32_e32 v3, v2
	v_mov_b32_e32 v4, v2
	v_mov_b32_e32 v5, v2
	v_mov_b32_e32 v6, v2
	v_mov_b32_e32 v7, v2
	v_mov_b32_e32 v8, v2
	v_mov_b32_e32 v9, v2
	v_mov_b32_e32 v10, v2
	v_mov_b32_e32 v11, v2
	v_mov_b32_e32 v12, v2
	v_mov_b32_e32 v13, v2
	v_mov_b32_e32 v14, v2
	v_mov_b32_e32 v15, v2
	v_mov_b32_e32 v16, v2
	v_mov_b32_e32 v17, v2
	v_mov_b32_e32 v26, v2
	v_mov_b32_e32 v27, v2
	v_mov_b32_e32 v28, v2
	v_mov_b32_e32 v29, v2
	v_mov_b32_e32 v30, v2
	v_mov_b32_e32 v31, v2
	v_mov_b32_e32 v32, v2
	v_mov_b32_e32 v33, v2
	v_mov_b32_e32 v42, v2
	v_mov_b32_e32 v43, v2
	v_mov_b32_e32 v44, v2
	v_mov_b32_e32 v45, v2
	v_mov_b32_e32 v46, v2
	v_mov_b32_e32 v47, v2
	v_mov_b32_e32 v48, v2
	v_mov_b32_e32 v49, v2
	v_mov_b32_e32 v18, v2
	v_mov_b32_e32 v19, v2
	v_mov_b32_e32 v20, v2
	v_mov_b32_e32 v21, v2
	v_mov_b32_e32 v22, v2
	v_mov_b32_e32 v23, v2
	v_mov_b32_e32 v24, v2
	v_mov_b32_e32 v25, v2
	v_mov_b32_e32 v34, v2
	v_mov_b32_e32 v35, v2
	v_mov_b32_e32 v36, v2
	v_mov_b32_e32 v37, v2
	v_mov_b32_e32 v38, v2
	v_mov_b32_e32 v39, v2
	v_mov_b32_e32 v40, v2
	v_mov_b32_e32 v41, v2
	v_mov_b32_e32 v50, v2
	v_mov_b32_e32 v51, v2
	v_mov_b32_e32 v52, v2
	v_mov_b32_e32 v53, v2
	v_mov_b32_e32 v54, v2
	v_mov_b32_e32 v55, v2
	v_mov_b32_e32 v56, v2
	v_mov_b32_e32 v57, v2
	v_mov_b32_e32 v58, v2
	v_mov_b32_e32 v59, v2
	v_mov_b32_e32 v60, v2
	v_mov_b32_e32 v61, v2
	v_mov_b32_e32 v62, v2
	v_mov_b32_e32 v63, v2
	v_mov_b32_e32 v64, v2
	v_mov_b32_e32 v65, v2
	v_mov_b32_e32 v66, v2
	v_mov_b32_e32 v67, v2
	v_mov_b32_e32 v68, v2
	v_mov_b32_e32 v69, v2
	v_mov_b32_e32 v70, v2
	v_mov_b32_e32 v71, v2
	v_mov_b32_e32 v72, v2
	v_mov_b32_e32 v73, v2
	v_mov_b32_e32 v74, v2
	v_mov_b32_e32 v75, v2
	v_mov_b32_e32 v76, v2
	v_mov_b32_e32 v77, v2
	v_mov_b32_e32 v78, v2
	v_mov_b32_e32 v79, v2
	v_mov_b32_e32 v80, v2
	v_mov_b32_e32 v81, v2
	v_mov_b32_e32 v90, v2
	v_mov_b32_e32 v91, v2
	v_mov_b32_e32 v92, v2
	v_mov_b32_e32 v93, v2
	v_mov_b32_e32 v94, v2
	v_mov_b32_e32 v95, v2
	v_mov_b32_e32 v96, v2
	v_mov_b32_e32 v97, v2
	v_mov_b32_e32 v106, v2
	v_mov_b32_e32 v107, v2
	v_mov_b32_e32 v108, v2
	v_mov_b32_e32 v109, v2
	v_mov_b32_e32 v110, v2
	v_mov_b32_e32 v111, v2
	v_mov_b32_e32 v112, v2
	v_mov_b32_e32 v113, v2
	v_mov_b32_e32 v82, v2
	v_mov_b32_e32 v83, v2
	v_mov_b32_e32 v84, v2
	v_mov_b32_e32 v85, v2
	v_mov_b32_e32 v86, v2
	v_mov_b32_e32 v87, v2
	v_mov_b32_e32 v88, v2
	v_mov_b32_e32 v89, v2
	v_mov_b32_e32 v98, v2
	v_mov_b32_e32 v99, v2
	v_mov_b32_e32 v100, v2
	v_mov_b32_e32 v101, v2
	v_mov_b32_e32 v102, v2
	v_mov_b32_e32 v103, v2
	v_mov_b32_e32 v104, v2
	v_mov_b32_e32 v105, v2
	v_mov_b32_e32 v114, v2
	v_mov_b32_e32 v115, v2
	v_mov_b32_e32 v116, v2
	v_mov_b32_e32 v117, v2
	v_mov_b32_e32 v118, v2
	v_mov_b32_e32 v119, v2
	v_mov_b32_e32 v120, v2
	v_mov_b32_e32 v121, v2
	v_mov_b32_e32 v122, v2
	v_mov_b32_e32 v123, v2
	v_mov_b32_e32 v124, v2
	v_mov_b32_e32 v125, v2
	v_mov_b32_e32 v126, v2
	v_mov_b32_e32 v127, v2
	v_mov_b32_e32 v128, v2
	v_mov_b32_e32 v129, v2
	v_add_u32_e32 v250, 0x18000, v147
	v_add_u32_e32 v251, 0x1c000, v147
.LBB0_1369:
	ds_read_b128 v[152:155], v149
	ds_read_b128 v[156:159], v149 offset:1024
	ds_read_b128 v[160:163], v149 offset:2048
	ds_read_b128 v[164:167], v149 offset:3072
	s_add_u32 s28, s26, 0xfff80080
	s_addc_u32 s29, s27, -1
	s_cmp_eq_u32 s54, 28
	s_cselect_b32 s31, s21, s29
	s_cselect_b32 s30, s50, s28
	s_cselect_b32 s29, s19, s53
	s_cselect_b32 s28, s51, s52
	s_add_i32 m0, s17, 0xc000
	ds_read_b128 v[168:171], v150
	ds_read_b128 v[172:175], v150 offset:1024
	ds_read_b128 v[176:179], v150 offset:2048
	ds_read_b128 v[180:183], v150 offset:3072
	ds_read_b128 v[184:187], v150 offset:4096
	ds_read_b128 v[190:193], v150 offset:5120
	ds_read_b128 v[194:197], v150 offset:6144
	ds_read_b128 v[198:201], v150 offset:7168
	global_load_lds_dwordx4 v138, s[26:27]
	s_add_i32 m0, s17, 0xe000
	s_nop 0
	global_load_lds_dwordx4 v140, s[26:27]
	s_waitcnt lgkmcnt(8)
	s_barrier
	s_waitcnt lgkmcnt(0)
	s_setprio 1
	s_waitcnt lgkmcnt(0)
	v_mfma_f32_16x16x32_bf16 v[126:129], v[152:155], v[168:171], v[126:129]
	v_mfma_f32_16x16x32_bf16 v[122:125], v[160:163], v[168:171], v[122:125]
	v_mfma_f32_16x16x32_bf16 v[118:121], v[152:155], v[176:179], v[118:121]
	v_mfma_f32_16x16x32_bf16 v[114:117], v[160:163], v[176:179], v[114:117]
	v_mfma_f32_16x16x32_bf16 v[102:105], v[152:155], v[184:187], v[102:105]
	v_mfma_f32_16x16x32_bf16 v[98:101], v[160:163], v[184:187], v[98:101]
	v_mfma_f32_16x16x32_bf16 v[86:89], v[152:155], v[194:197], v[86:89]
	v_mfma_f32_16x16x32_bf16 v[82:85], v[160:163], v[194:197], v[82:85]
	v_mfma_f32_16x16x32_bf16 v[126:129], v[156:159], v[172:175], v[126:129]
	v_mfma_f32_16x16x32_bf16 v[122:125], v[164:167], v[172:175], v[122:125]
	v_mfma_f32_16x16x32_bf16 v[118:121], v[156:159], v[180:183], v[118:121]
	v_mfma_f32_16x16x32_bf16 v[114:117], v[164:167], v[180:183], v[114:117]
	v_mfma_f32_16x16x32_bf16 v[102:105], v[156:159], v[190:193], v[102:105]
	v_mfma_f32_16x16x32_bf16 v[98:101], v[164:167], v[190:193], v[98:101]
	v_mfma_f32_16x16x32_bf16 v[86:89], v[156:159], v[198:201], v[86:89]
	v_mfma_f32_16x16x32_bf16 v[82:85], v[164:167], v[198:201], v[82:85]
	s_setprio 0
	s_barrier
	s_add_i32 s55, s43, s35
	s_add_u32 s66, s28, 0x80
	s_addc_u32 s67, s29, 0
	s_mov_b32 m0, s55
	ds_read_b128 v[214:217], v151
	ds_read_b128 v[218:221], v151 offset:1024
	ds_read_b128 v[222:225], v151 offset:2048
	ds_read_b128 v[226:229], v151 offset:3072
	global_load_lds_dwordx4 v132, s[28:29]
	s_add_i32 m0, s55, 0x2000
	s_nop 0
	global_load_lds_dwordx4 v136, s[28:29]
	s_barrier
	s_waitcnt lgkmcnt(0)
	s_setprio 1
	s_waitcnt lgkmcnt(0)
	v_mfma_f32_16x16x32_bf16 v[110:113], v[214:217], v[168:171], v[110:113]
	v_mfma_f32_16x16x32_bf16 v[106:109], v[222:225], v[168:171], v[106:109]
	v_mfma_f32_16x16x32_bf16 v[94:97], v[214:217], v[176:179], v[94:97]
	v_mfma_f32_16x16x32_bf16 v[90:93], v[222:225], v[176:179], v[90:93]
	v_mfma_f32_16x16x32_bf16 v[78:81], v[214:217], v[184:187], v[78:81]
	v_mfma_f32_16x16x32_bf16 v[74:77], v[222:225], v[184:187], v[74:77]
	v_mfma_f32_16x16x32_bf16 v[70:73], v[214:217], v[194:197], v[70:73]
	v_mfma_f32_16x16x32_bf16 v[66:69], v[222:225], v[194:197], v[66:69]
	v_mfma_f32_16x16x32_bf16 v[110:113], v[218:221], v[172:175], v[110:113]
	v_mfma_f32_16x16x32_bf16 v[106:109], v[226:229], v[172:175], v[106:109]
	v_mfma_f32_16x16x32_bf16 v[94:97], v[218:221], v[180:183], v[94:97]
	v_mfma_f32_16x16x32_bf16 v[90:93], v[226:229], v[180:183], v[90:93]
	v_mfma_f32_16x16x32_bf16 v[78:81], v[218:221], v[190:193], v[78:81]
	v_mfma_f32_16x16x32_bf16 v[74:77], v[226:229], v[190:193], v[74:77]
	v_mfma_f32_16x16x32_bf16 v[70:73], v[218:221], v[198:201], v[70:73]
	v_mfma_f32_16x16x32_bf16 v[66:69], v[226:229], v[198:201], v[66:69]
	s_setprio 0
	s_mov_b32 m0, s17
	s_add_u32 s68, s30, 0x80
	s_addc_u32 s69, s31, 0
	s_barrier
	ds_read_b128 v[168:171], v150 offset:16384
	ds_read_b128 v[172:175], v150 offset:17408
	ds_read_b128 v[176:179], v150 offset:18432
	ds_read_b128 v[180:183], v150 offset:19456
	ds_read_b128 v[184:187], v150 offset:20480
	ds_read_b128 v[190:193], v150 offset:21504
	ds_read_b128 v[194:197], v150 offset:22528
	ds_read_b128 v[198:201], v150 offset:23552
	global_load_lds_dwordx4 v130, s[30:31]
	s_mov_b32 m0, s36
	s_nop 0
	global_load_lds_dwordx4 v134, s[30:31]
	s_barrier
	s_waitcnt lgkmcnt(0)
	s_setprio 1
	s_waitcnt lgkmcnt(0)
	v_mfma_f32_16x16x32_bf16 v[62:65], v[152:155], v[168:171], v[62:65]
	v_mfma_f32_16x16x32_bf16 v[58:61], v[160:163], v[168:171], v[58:61]
	v_mfma_f32_16x16x32_bf16 v[54:57], v[152:155], v[176:179], v[54:57]
	v_mfma_f32_16x16x32_bf16 v[50:53], v[160:163], v[176:179], v[50:53]
	v_mfma_f32_16x16x32_bf16 v[38:41], v[152:155], v[184:187], v[38:41]
	v_mfma_f32_16x16x32_bf16 v[34:37], v[160:163], v[184:187], v[34:37]
	v_mfma_f32_16x16x32_bf16 v[22:25], v[152:155], v[194:197], v[22:25]
	v_mfma_f32_16x16x32_bf16 v[18:21], v[160:163], v[194:197], v[18:21]
	v_mfma_f32_16x16x32_bf16 v[62:65], v[156:159], v[172:175], v[62:65]
	v_mfma_f32_16x16x32_bf16 v[58:61], v[164:167], v[172:175], v[58:61]
	v_mfma_f32_16x16x32_bf16 v[54:57], v[156:159], v[180:183], v[54:57]
	v_mfma_f32_16x16x32_bf16 v[50:53], v[164:167], v[180:183], v[50:53]
	v_mfma_f32_16x16x32_bf16 v[38:41], v[156:159], v[190:193], v[38:41]
	v_mfma_f32_16x16x32_bf16 v[34:37], v[164:167], v[190:193], v[34:37]
	v_mfma_f32_16x16x32_bf16 v[22:25], v[156:159], v[198:201], v[22:25]
	v_mfma_f32_16x16x32_bf16 v[18:21], v[164:167], v[198:201], v[18:21]
	s_setprio 0
	s_barrier
	s_add_u32 s56, s28, 0x80000
	s_addc_u32 s57, s29, 0
	s_add_i32 s55, s44, s35
	s_mov_b32 m0, s55
	s_nop 0
	global_load_lds_dwordx4 v132, s[56:57]
	s_add_i32 m0, s55, 0x2000
	s_nop 0
	global_load_lds_dwordx4 v136, s[56:57]
	s_waitcnt vmcnt(6)
	s_barrier
	s_setprio 1
	v_mfma_f32_16x16x32_bf16 v[46:49], v[214:217], v[168:171], v[46:49]
	v_mfma_f32_16x16x32_bf16 v[42:45], v[222:225], v[168:171], v[42:45]
	v_mfma_f32_16x16x32_bf16 v[30:33], v[214:217], v[176:179], v[30:33]
	v_mfma_f32_16x16x32_bf16 v[26:29], v[222:225], v[176:179], v[26:29]
	v_mfma_f32_16x16x32_bf16 v[14:17], v[214:217], v[184:187], v[14:17]
	v_mfma_f32_16x16x32_bf16 v[10:13], v[222:225], v[184:187], v[10:13]
	v_mfma_f32_16x16x32_bf16 v[6:9], v[214:217], v[194:197], v[6:9]
	v_mfma_f32_16x16x32_bf16 v[2:5], v[222:225], v[194:197], v[2:5]
	v_mfma_f32_16x16x32_bf16 v[46:49], v[218:221], v[172:175], v[46:49]
	v_mfma_f32_16x16x32_bf16 v[42:45], v[226:229], v[172:175], v[42:45]
	v_mfma_f32_16x16x32_bf16 v[30:33], v[218:221], v[180:183], v[30:33]
	v_mfma_f32_16x16x32_bf16 v[26:29], v[226:229], v[180:183], v[26:29]
	v_mfma_f32_16x16x32_bf16 v[14:17], v[218:221], v[190:193], v[14:17]
	v_mfma_f32_16x16x32_bf16 v[10:13], v[226:229], v[190:193], v[10:13]
	v_mfma_f32_16x16x32_bf16 v[6:9], v[218:221], v[198:201], v[6:9]
	v_mfma_f32_16x16x32_bf16 v[2:5], v[226:229], v[198:201], v[2:5]
	s_setprio 0
	s_add_i32 s55, 0, 0x18000
	s_barrier
	ds_read_b128 v[152:155], v250
	ds_read_b128 v[156:159], v250 offset:1024
	ds_read_b128 v[160:163], v250 offset:2048
	ds_read_b128 v[164:167], v250 offset:3072
	s_add_u32 s30, s30, 0x80000
	s_addc_u32 s31, s31, 0
	s_mov_b32 m0, s37
	ds_read_b128 v[168:171], v150 offset:32768
	ds_read_b128 v[172:175], v150 offset:33792
	ds_read_b128 v[176:179], v150 offset:34816
	ds_read_b128 v[180:183], v150 offset:35840
	ds_read_b128 v[184:187], v150 offset:36864
	ds_read_b128 v[190:193], v150 offset:37888
	ds_read_b128 v[194:197], v150 offset:38912
	ds_read_b128 v[198:201], v150 offset:39936
	global_load_lds_dwordx4 v130, s[30:31]
	s_mov_b32 m0, s38
	s_nop 0
	global_load_lds_dwordx4 v134, s[30:31]
	s_waitcnt lgkmcnt(8)
	s_barrier
	s_waitcnt lgkmcnt(0)
	s_setprio 1
	s_waitcnt lgkmcnt(0)
	v_mfma_f32_16x16x32_bf16 v[126:129], v[152:155], v[168:171], v[126:129]
	v_mfma_f32_16x16x32_bf16 v[122:125], v[160:163], v[168:171], v[122:125]
	v_mfma_f32_16x16x32_bf16 v[118:121], v[152:155], v[176:179], v[118:121]
	v_mfma_f32_16x16x32_bf16 v[114:117], v[160:163], v[176:179], v[114:117]
	v_mfma_f32_16x16x32_bf16 v[102:105], v[152:155], v[184:187], v[102:105]
	v_mfma_f32_16x16x32_bf16 v[98:101], v[160:163], v[184:187], v[98:101]
	v_mfma_f32_16x16x32_bf16 v[86:89], v[152:155], v[194:197], v[86:89]
	v_mfma_f32_16x16x32_bf16 v[82:85], v[160:163], v[194:197], v[82:85]
	v_mfma_f32_16x16x32_bf16 v[126:129], v[156:159], v[172:175], v[126:129]
	v_mfma_f32_16x16x32_bf16 v[122:125], v[164:167], v[172:175], v[122:125]
	v_mfma_f32_16x16x32_bf16 v[118:121], v[156:159], v[180:183], v[118:121]
	v_mfma_f32_16x16x32_bf16 v[114:117], v[164:167], v[180:183], v[114:117]
	v_mfma_f32_16x16x32_bf16 v[102:105], v[156:159], v[190:193], v[102:105]
	v_mfma_f32_16x16x32_bf16 v[98:101], v[164:167], v[190:193], v[98:101]
	v_mfma_f32_16x16x32_bf16 v[86:89], v[156:159], v[198:201], v[86:89]
	v_mfma_f32_16x16x32_bf16 v[82:85], v[164:167], v[198:201], v[82:85]
	s_setprio 0
	s_barrier
	s_add_i32 s30, 0, 0x1c000
	s_add_i32 s31, s55, s35
	s_mov_b32 m0, s31
	ds_read_b128 v[214:217], v251
	ds_read_b128 v[218:221], v251 offset:1024
	ds_read_b128 v[222:225], v251 offset:2048
	ds_read_b128 v[226:229], v251 offset:3072
	global_load_lds_dwordx4 v132, s[66:67]
	s_add_i32 m0, s31, 0x2000
	s_nop 0
	global_load_lds_dwordx4 v136, s[66:67]
	s_barrier
	s_waitcnt lgkmcnt(0)
	s_setprio 1
	s_waitcnt lgkmcnt(0)
	v_mfma_f32_16x16x32_bf16 v[110:113], v[214:217], v[168:171], v[110:113]
	v_mfma_f32_16x16x32_bf16 v[106:109], v[222:225], v[168:171], v[106:109]
	v_mfma_f32_16x16x32_bf16 v[94:97], v[214:217], v[176:179], v[94:97]
	v_mfma_f32_16x16x32_bf16 v[90:93], v[222:225], v[176:179], v[90:93]
	v_mfma_f32_16x16x32_bf16 v[78:81], v[214:217], v[184:187], v[78:81]
	v_mfma_f32_16x16x32_bf16 v[74:77], v[222:225], v[184:187], v[74:77]
	v_mfma_f32_16x16x32_bf16 v[70:73], v[214:217], v[194:197], v[70:73]
	v_mfma_f32_16x16x32_bf16 v[66:69], v[222:225], v[194:197], v[66:69]
	v_mfma_f32_16x16x32_bf16 v[110:113], v[218:221], v[172:175], v[110:113]
	v_mfma_f32_16x16x32_bf16 v[106:109], v[226:229], v[172:175], v[106:109]
	v_mfma_f32_16x16x32_bf16 v[94:97], v[218:221], v[180:183], v[94:97]
	v_mfma_f32_16x16x32_bf16 v[90:93], v[226:229], v[180:183], v[90:93]
	v_mfma_f32_16x16x32_bf16 v[78:81], v[218:221], v[190:193], v[78:81]
	v_mfma_f32_16x16x32_bf16 v[74:77], v[226:229], v[190:193], v[74:77]
	v_mfma_f32_16x16x32_bf16 v[70:73], v[218:221], v[198:201], v[70:73]
	v_mfma_f32_16x16x32_bf16 v[66:69], v[226:229], v[198:201], v[66:69]
	s_setprio 0
	s_mov_b32 m0, s40
	s_barrier
	ds_read_b128 v[168:171], v150 offset:49152
	ds_read_b128 v[172:175], v150 offset:50176
	ds_read_b128 v[176:179], v150 offset:51200
	ds_read_b128 v[180:183], v150 offset:52224
	ds_read_b128 v[184:187], v150 offset:53248
	ds_read_b128 v[190:193], v150 offset:54272
	ds_read_b128 v[194:197], v150 offset:55296
	ds_read_b128 v[198:201], v150 offset:56320
	global_load_lds_dwordx4 v130, s[68:69]
	s_mov_b32 m0, s41
	s_nop 0
	global_load_lds_dwordx4 v134, s[68:69]
	s_barrier
	s_waitcnt lgkmcnt(0)
	s_setprio 1
	s_waitcnt lgkmcnt(0)
	v_mfma_f32_16x16x32_bf16 v[62:65], v[152:155], v[168:171], v[62:65]
	v_mfma_f32_16x16x32_bf16 v[58:61], v[160:163], v[168:171], v[58:61]
	v_mfma_f32_16x16x32_bf16 v[54:57], v[152:155], v[176:179], v[54:57]
	v_mfma_f32_16x16x32_bf16 v[50:53], v[160:163], v[176:179], v[50:53]
	v_mfma_f32_16x16x32_bf16 v[38:41], v[152:155], v[184:187], v[38:41]
	v_mfma_f32_16x16x32_bf16 v[34:37], v[160:163], v[184:187], v[34:37]
	v_mfma_f32_16x16x32_bf16 v[22:25], v[152:155], v[194:197], v[22:25]
	v_mfma_f32_16x16x32_bf16 v[18:21], v[160:163], v[194:197], v[18:21]
	v_mfma_f32_16x16x32_bf16 v[62:65], v[156:159], v[172:175], v[62:65]
	v_mfma_f32_16x16x32_bf16 v[58:61], v[164:167], v[172:175], v[58:61]
	v_mfma_f32_16x16x32_bf16 v[54:57], v[156:159], v[180:183], v[54:57]
	v_mfma_f32_16x16x32_bf16 v[50:53], v[164:167], v[180:183], v[50:53]
	v_mfma_f32_16x16x32_bf16 v[38:41], v[156:159], v[190:193], v[38:41]
	v_mfma_f32_16x16x32_bf16 v[34:37], v[164:167], v[190:193], v[34:37]
	v_mfma_f32_16x16x32_bf16 v[22:25], v[156:159], v[198:201], v[22:25]
	v_mfma_f32_16x16x32_bf16 v[18:21], v[164:167], v[198:201], v[18:21]
	s_setprio 0
	s_barrier
	s_add_u32 s28, s28, 0x80080
	s_addc_u32 s29, s29, 0
	s_add_i32 s30, s30, s35
	s_mov_b32 m0, s30
	s_nop 0
	global_load_lds_dwordx4 v132, s[28:29]
	s_add_i32 m0, s30, 0x2000
	s_nop 0
	global_load_lds_dwordx4 v136, s[28:29]
	s_waitcnt vmcnt(6)
	s_barrier
	s_setprio 1
	v_mfma_f32_16x16x32_bf16 v[46:49], v[214:217], v[168:171], v[46:49]
	v_mfma_f32_16x16x32_bf16 v[42:45], v[222:225], v[168:171], v[42:45]
	v_mfma_f32_16x16x32_bf16 v[30:33], v[214:217], v[176:179], v[30:33]
	v_mfma_f32_16x16x32_bf16 v[26:29], v[222:225], v[176:179], v[26:29]
	v_mfma_f32_16x16x32_bf16 v[14:17], v[214:217], v[184:187], v[14:17]
	v_mfma_f32_16x16x32_bf16 v[10:13], v[222:225], v[184:187], v[10:13]
	v_mfma_f32_16x16x32_bf16 v[6:9], v[214:217], v[194:197], v[6:9]
	v_mfma_f32_16x16x32_bf16 v[2:5], v[222:225], v[194:197], v[2:5]
	v_mfma_f32_16x16x32_bf16 v[46:49], v[218:221], v[172:175], v[46:49]
	v_mfma_f32_16x16x32_bf16 v[42:45], v[226:229], v[172:175], v[42:45]
	v_mfma_f32_16x16x32_bf16 v[30:33], v[218:221], v[180:183], v[30:33]
	v_mfma_f32_16x16x32_bf16 v[26:29], v[226:229], v[180:183], v[26:29]
	v_mfma_f32_16x16x32_bf16 v[14:17], v[218:221], v[190:193], v[14:17]
	v_mfma_f32_16x16x32_bf16 v[10:13], v[226:229], v[190:193], v[10:13]
	v_mfma_f32_16x16x32_bf16 v[6:9], v[218:221], v[198:201], v[6:9]
	v_mfma_f32_16x16x32_bf16 v[2:5], v[226:229], v[198:201], v[2:5]
	s_setprio 0
	s_add_i32 s54, s54, 2
	s_add_u32 s26, s26, 0x100
	s_addc_u32 s27, s27, 0
	s_add_u32 s52, s52, 0x100
	s_addc_u32 s53, s53, 0
	s_cmp_gt_u32 s54, 29
	s_barrier
	s_cbranch_scc0 .LBB0_1369
	v_lshl_add_u32 v152, s16, 8, v146
	v_lshl_or_b32 v154, s49, 8, v148
	v_ashrrev_i32_e32 v153, 31, v152
	v_ashrrev_i32_e32 v155, 31, v154
	v_lshlrev_b64 v[156:157], 12, v[152:153]
	v_lshl_add_u64 v[156:157], s[96:97], 0, v[156:157]
	v_lshlrev_b64 v[154:155], 1, v[154:155]
	v_lshl_add_u64 v[156:157], v[156:157], 0, v[154:155]
	v_cvt_pk_bf16_f32 v62, v62, v63
	v_cvt_pk_bf16_f32 v63, v64, v65
	v_cvt_pk_bf16_f32 v64, v58, v59
	v_add_co_u32_e32 v58, vcc, s45, v156
	v_cvt_pk_bf16_f32 v70, v70, v71
	v_cvt_pk_bf16_f32 v71, v72, v73
	v_cvt_pk_bf16_f32 v72, v66, v67
	v_lshl_add_u64 v[66:67], v[156:157], 0, s[6:7]
	v_addc_co_u32_e32 v59, vcc, 0, v157, vcc
	v_cvt_pk_bf16_f32 v46, v46, v47
	v_cvt_pk_bf16_f32 v47, v48, v49
	v_cvt_pk_bf16_f32 v48, v42, v43
	v_cvt_pk_bf16_f32 v49, v44, v45
	v_cvt_pk_bf16_f32 v110, v110, v111
	v_cvt_pk_bf16_f32 v111, v112, v113
	v_cvt_pk_bf16_f32 v112, v106, v107
	v_or_b32_e32 v106, 16, v152
	global_store_dwordx4 v[66:67], v[46:49], off offset:256
	v_ashrrev_i32_e32 v107, 31, v106
	v_cvt_pk_bf16_f32 v94, v94, v95
	v_add_co_u32_e32 v48, vcc, s46, v156
	v_cvt_pk_bf16_f32 v95, v96, v97
	v_cvt_pk_bf16_f32 v96, v90, v91
	v_or_b32_e32 v90, 32, v152
	v_lshl_add_u64 v[46:47], v[156:157], 0, s[10:11]
	v_addc_co_u32_e32 v49, vcc, 0, v157, vcc
	v_cvt_pk_bf16_f32 v30, v30, v31
	v_cvt_pk_bf16_f32 v31, v32, v33
	v_cvt_pk_bf16_f32 v32, v26, v27
	v_cvt_pk_bf16_f32 v33, v28, v29
	v_lshlrev_b64 v[106:107], 12, v[106:107]
	v_ashrrev_i32_e32 v91, 31, v90
	v_cvt_pk_bf16_f32 v78, v78, v79
	v_cvt_pk_bf16_f32 v79, v80, v81
	v_cvt_pk_bf16_f32 v80, v74, v75
	v_or_b32_e32 v74, 48, v152
	global_store_dwordx4 v[46:47], v[30:33], off offset:256
	v_cvt_pk_bf16_f32 v113, v108, v109
	v_lshl_add_u64 v[106:107], s[96:97], 0, v[106:107]
	v_add_co_u32_e32 v32, vcc, s47, v156
	v_lshlrev_b64 v[90:91], 12, v[90:91]
	v_ashrrev_i32_e32 v75, 31, v74
	v_lshl_add_u64 v[30:31], v[156:157], 0, s[12:13]
	v_addc_co_u32_e32 v33, vcc, 0, v157, vcc
	v_cvt_pk_bf16_f32 v14, v14, v15
	v_cvt_pk_bf16_f32 v15, v16, v17
	v_cvt_pk_bf16_f32 v16, v10, v11
	v_cvt_pk_bf16_f32 v17, v12, v13
	global_store_dwordx4 v[156:157], v[110:113], off offset:256
	v_cvt_pk_bf16_f32 v97, v92, v93
	v_lshl_add_u64 v[90:91], s[96:97], 0, v[90:91]
	v_lshl_add_u64 v[110:111], v[106:107], 0, v[154:155]
	v_lshlrev_b64 v[74:75], 12, v[74:75]
	global_store_dwordx4 v[30:31], v[14:17], off offset:256
	global_store_dwordx4 v[110:111], v[94:97], off offset:256
	v_cvt_pk_bf16_f32 v81, v76, v77
	v_add_co_u32_e32 v16, vcc, s48, v156
	v_lshl_add_u64 v[94:95], v[90:91], 0, v[154:155]
	v_lshl_add_u64 v[74:75], s[96:97], 0, v[74:75]
	v_addc_co_u32_e32 v17, vcc, 0, v157, vcc
	v_cvt_pk_bf16_f32 v126, v126, v127
	v_cvt_pk_bf16_f32 v127, v128, v129
	v_cvt_pk_bf16_f32 v128, v122, v123
	v_cvt_pk_bf16_f32 v129, v124, v125
	v_cvt_pk_bf16_f32 v106, v118, v119
	v_cvt_pk_bf16_f32 v107, v120, v121
	v_cvt_pk_bf16_f32 v108, v114, v115
	v_cvt_pk_bf16_f32 v109, v116, v117
	v_cvt_pk_bf16_f32 v90, v102, v103
	v_cvt_pk_bf16_f32 v91, v104, v105
	v_cvt_pk_bf16_f32 v92, v98, v99
	v_cvt_pk_bf16_f32 v93, v100, v101
	global_store_dwordx4 v[94:95], v[78:81], off offset:256
	v_cvt_pk_bf16_f32 v76, v82, v83
	v_cvt_pk_bf16_f32 v77, v84, v85
	v_lshl_add_u64 v[78:79], v[74:75], 0, v[154:155]
	v_cvt_pk_bf16_f32 v74, v86, v87
	v_cvt_pk_bf16_f32 v75, v88, v89
	v_cvt_pk_bf16_f32 v73, v68, v69
	v_cvt_pk_bf16_f32 v65, v60, v61
	v_cvt_pk_bf16_f32 v42, v54, v55
	v_cvt_pk_bf16_f32 v43, v56, v57
	v_cvt_pk_bf16_f32 v44, v50, v51
	v_cvt_pk_bf16_f32 v45, v52, v53
	v_cvt_pk_bf16_f32 v26, v38, v39
	v_cvt_pk_bf16_f32 v27, v40, v41
	v_cvt_pk_bf16_f32 v28, v34, v35
	v_cvt_pk_bf16_f32 v29, v36, v37
	v_lshl_add_u64 v[14:15], v[156:157], 0, s[14:15]
	v_cvt_pk_bf16_f32 v10, v22, v23
	v_cvt_pk_bf16_f32 v11, v24, v25
	v_cvt_pk_bf16_f32 v12, v18, v19
	v_cvt_pk_bf16_f32 v13, v20, v21
	v_cvt_pk_bf16_f32 v6, v6, v7
	v_cvt_pk_bf16_f32 v7, v8, v9
	v_cvt_pk_bf16_f32 v8, v2, v3
	v_cvt_pk_bf16_f32 v9, v4, v5
	s_and_b64 vcc, exec, s[0:1]
	s_mov_b32 s49, s18
	s_mov_b32 s16, s20
	s_mov_b64 s[28:29], s[24:25]
	s_mov_b64 s[26:27], s[22:23]
	global_store_dwordx4 v[156:157], v[126:129], off
	global_store_dwordx4 v[110:111], v[106:109], off
	global_store_dwordx4 v[94:95], v[90:93], off
	global_store_dwordx4 v[78:79], v[74:77], off
	global_store_dwordx4 v[78:79], v[70:73], off offset:256
	global_store_dwordx4 v[58:59], v[62:65], off
	global_store_dwordx4 v[48:49], v[42:45], off
	global_store_dwordx4 v[32:33], v[26:29], off
	global_store_dwordx4 v[16:17], v[10:13], off
	global_store_dwordx4 v[14:15], v[6:9], off offset:256
	s_cbranch_vccz .LBB0_1362
	s_waitcnt vmcnt(0)
	s_cmpk_gt_u32 s2, 0xff
	s_cbranch_scc1 .LBB0_1373
	s_barrier
